# L1+L2: ds_swizzle broadcasts -> DPP (folded into address adds), LDS waitcnts re-derived
# baseline (speedup 1.0000x reference)
.Lp1_after_idx:
	s_waitcnt vmcnt(0)
	v_lshrrev_b32_e32 v36, 10, v36
	v_lshrrev_b32_e32 v68, 10, v68
	v_lshrrev_b32_e32 v74, 10, v74
	v_lshrrev_b32_e32 v85, 10, v85
	v_lshrrev_b32_e32 v84, 10, v84
	v_lshrrev_b32_e32 v109, 10, v109
	v_lshrrev_b32_e32 v107, 10, v107
	v_lshrrev_b32_e32 v106, 10, v106
	v_lshrrev_b32_e32 v95, 10, v95
	v_and_b32_e32 v36, 0x3fff80, v36
	v_and_b32_e32 v68, 0x3fff80, v68
	v_and_b32_e32 v74, 0x3fff80, v74
	v_and_b32_e32 v85, 0x3fff80, v85
	v_and_b32_e32 v84, 0x3fff80, v84
	v_and_b32_e32 v109, 0x3fff80, v109
	v_and_b32_e32 v107, 0x3fff80, v107
	v_and_b32_e32 v106, 0x3fff80, v106
	v_and_b32_e32 v95, 0x3fff80, v95
	v_mov_b32_dpp v41, v36 row_newbcast:6 row_mask:0xf bank_mask:0x3
	v_mov_b32_dpp v41, v36 row_newbcast:14 row_mask:0xf bank_mask:0xc
	v_add_u32_dpp v37, v36, v102 row_newbcast:0 row_mask:0xf bank_mask:0x3
	v_add_u32_dpp v37, v36, v102 row_newbcast:8 row_mask:0xf bank_mask:0xc
	v_add_u32_dpp v38, v36, v102 row_newbcast:1 row_mask:0xf bank_mask:0x3
	v_add_u32_dpp v38, v36, v102 row_newbcast:9 row_mask:0xf bank_mask:0xc
	ds_read_b128 v[60:63], v37 offset:52240
	ds_read_b128 v[52:55], v38 offset:52240
	v_add_u32_dpp v37, v36, v102 row_newbcast:2 row_mask:0xf bank_mask:0x3
	v_add_u32_dpp v37, v36, v102 row_newbcast:10 row_mask:0xf bank_mask:0xc
	v_add_u32_dpp v39, v36, v102 row_newbcast:3 row_mask:0xf bank_mask:0x3
	v_add_u32_dpp v39, v36, v102 row_newbcast:11 row_mask:0xf bank_mask:0xc
	v_mov_b32_dpp v40, v36 row_newbcast:5 row_mask:0xf bank_mask:0x3
	v_mov_b32_dpp v40, v36 row_newbcast:13 row_mask:0xf bank_mask:0xc
	v_mov_b32_dpp v42, v36 row_newbcast:7 row_mask:0xf bank_mask:0x3
	v_mov_b32_dpp v42, v36 row_newbcast:15 row_mask:0xf bank_mask:0xc
	ds_read_b128 v[64:67], v37 offset:52240
	ds_read_b128 v[56:59], v39 offset:52240
	v_add_u32_dpp v37, v36, v102 row_newbcast:4 row_mask:0xf bank_mask:0x3
	v_add_u32_dpp v37, v36, v102 row_newbcast:12 row_mask:0xf bank_mask:0xc
	v_cmp_lt_i32_e32 vcc, 8, v72
	v_add_u32_e32 v36, v102, v40
	v_add_u32_e32 v40, v102, v41
	v_add_u32_e32 v41, v102, v42
	ds_read_b128 v[44:47], v37 offset:52240
	ds_read_b128 v[36:39], v36 offset:52240
	ds_read_b128 v[48:51], v40 offset:52240
	ds_read_b128 v[40:43], v41 offset:52240
	s_cmp_lg_u64 vcc, 0
	s_cselect_b64 s[22:23], -1, 0
	v_cmp_lt_i32_e64 s[6:7], 12, v72
	s_cbranch_vccz .LBB4_44
	v_add_u32_dpp v0, v68, v102 row_newbcast:0 row_mask:0xf bank_mask:0x3
	v_add_u32_dpp v0, v68, v102 row_newbcast:8 row_mask:0xf bank_mask:0xc
	v_add_u32_dpp v8, v68, v102 row_newbcast:1 row_mask:0xf bank_mask:0x3
	v_add_u32_dpp v8, v68, v102 row_newbcast:9 row_mask:0xf bank_mask:0xc
	v_add_u32_dpp v16, v68, v102 row_newbcast:2 row_mask:0xf bank_mask:0x3
	v_add_u32_dpp v16, v68, v102 row_newbcast:10 row_mask:0xf bank_mask:0xc
	v_add_u32_dpp v24, v68, v102 row_newbcast:3 row_mask:0xf bank_mask:0x3
	v_add_u32_dpp v24, v68, v102 row_newbcast:11 row_mask:0xf bank_mask:0xc
	ds_read_b128 v[0:3], v0 offset:52240
	ds_read_b128 v[8:11], v8 offset:52240
	ds_read_b128 v[16:19], v16 offset:52240
	ds_read_b128 v[24:27], v24 offset:52240
.LBB4_44:
	s_cmp_lg_u64 s[6:7], 0
	s_cselect_b64 s[26:27], -1, 0
	s_cmp_eq_u64 s[6:7], 0
	s_cbranch_scc1 .LBB4_46
	v_add_u32_dpp v4, v68, v102 row_newbcast:4 row_mask:0xf bank_mask:0x3
	v_add_u32_dpp v4, v68, v102 row_newbcast:12 row_mask:0xf bank_mask:0xc
	v_add_u32_dpp v12, v68, v102 row_newbcast:5 row_mask:0xf bank_mask:0x3
	v_add_u32_dpp v12, v68, v102 row_newbcast:13 row_mask:0xf bank_mask:0xc
	v_add_u32_dpp v20, v68, v102 row_newbcast:6 row_mask:0xf bank_mask:0x3
	v_add_u32_dpp v20, v68, v102 row_newbcast:14 row_mask:0xf bank_mask:0xc
	v_add_u32_dpp v28, v68, v102 row_newbcast:7 row_mask:0xf bank_mask:0x3
	v_add_u32_dpp v28, v68, v102 row_newbcast:15 row_mask:0xf bank_mask:0xc
	ds_read_b128 v[4:7], v4 offset:52240
	ds_read_b128 v[12:15], v12 offset:52240
	ds_read_b128 v[20:23], v20 offset:52240
	ds_read_b128 v[28:31], v28 offset:52240

.LBB4_50:
	v_cmp_lt_i32_e32 vcc, 16, v72
	s_cbranch_vccz .LBB4_61
	v_cmp_lt_i32_e32 vcc, 20, v72
	v_add_u32_dpp v56, v74, v102 row_newbcast:0 row_mask:0xf bank_mask:0x3
	v_add_u32_dpp v56, v74, v102 row_newbcast:8 row_mask:0xf bank_mask:0xc
	v_add_u32_dpp v57, v74, v102 row_newbcast:1 row_mask:0xf bank_mask:0x3
	v_add_u32_dpp v57, v74, v102 row_newbcast:9 row_mask:0xf bank_mask:0xc
	ds_read_b128 v[68:71], v56 offset:52240
	ds_read_b128 v[64:67], v57 offset:52240
	v_add_u32_dpp v56, v74, v102 row_newbcast:2 row_mask:0xf bank_mask:0x3
	v_add_u32_dpp v56, v74, v102 row_newbcast:10 row_mask:0xf bank_mask:0xc
	v_add_u32_dpp v57, v74, v102 row_newbcast:3 row_mask:0xf bank_mask:0x3
	v_add_u32_dpp v57, v74, v102 row_newbcast:11 row_mask:0xf bank_mask:0xc
	ds_read_b128 v[60:63], v56 offset:52240
	ds_read_b128 v[56:59], v57 offset:52240
	s_cmp_lg_u64 vcc, 0
	s_cselect_b64 s[6:7], -1, 0
	s_cbranch_vccz .LBB4_53
	v_add_u32_dpp v36, v74, v102 row_newbcast:4 row_mask:0xf bank_mask:0x3
	v_add_u32_dpp v36, v74, v102 row_newbcast:12 row_mask:0xf bank_mask:0xc
	v_add_u32_dpp v37, v74, v102 row_newbcast:5 row_mask:0xf bank_mask:0x3
	v_add_u32_dpp v37, v74, v102 row_newbcast:13 row_mask:0xf bank_mask:0xc
	v_add_u32_dpp v40, v74, v102 row_newbcast:6 row_mask:0xf bank_mask:0x3
	v_add_u32_dpp v40, v74, v102 row_newbcast:14 row_mask:0xf bank_mask:0xc
	v_add_u32_dpp v41, v74, v102 row_newbcast:7 row_mask:0xf bank_mask:0x3
	v_add_u32_dpp v41, v74, v102 row_newbcast:15 row_mask:0xf bank_mask:0xc
	ds_read_b128 v[44:47], v36 offset:52240
	ds_read_b128 v[36:39], v37 offset:52240
	ds_read_b128 v[48:51], v40 offset:52240
	ds_read_b128 v[40:43], v41 offset:52240

.LBB4_56:
	s_waitcnt lgkmcnt(0)
	s_or_b64 exec, exec, s[6:7]
	s_nop 1
	v_add_u32_dpp v37, v36, v102 row_newbcast:0 row_mask:0xf bank_mask:0x3
	v_add_u32_dpp v37, v36, v102 row_newbcast:8 row_mask:0xf bank_mask:0xc
	v_add_u32_dpp v42, v36, v102 row_newbcast:1 row_mask:0xf bank_mask:0x3
	v_add_u32_dpp v42, v36, v102 row_newbcast:9 row_mask:0xf bank_mask:0xc
	ds_read_b128 v[38:41], v37 offset:52240
	ds_read_b128 v[42:45], v42 offset:52240
	v_add_u32_dpp v37, v36, v102 row_newbcast:2 row_mask:0xf bank_mask:0x3
	v_add_u32_dpp v37, v36, v102 row_newbcast:10 row_mask:0xf bank_mask:0xc
	v_add_u32_dpp v51, v36, v102 row_newbcast:3 row_mask:0xf bank_mask:0x3
	v_add_u32_dpp v51, v36, v102 row_newbcast:11 row_mask:0xf bank_mask:0xc
	v_mov_b32_dpp v60, v36 row_newbcast:5 row_mask:0xf bank_mask:0x3
	v_mov_b32_dpp v60, v36 row_newbcast:13 row_mask:0xf bank_mask:0xc
	ds_read_b128 v[46:49], v37 offset:52240
	ds_read_b128 v[56:59], v51 offset:52240
	v_add_u32_dpp v37, v36, v102 row_newbcast:4 row_mask:0xf bank_mask:0x3
	v_add_u32_dpp v37, v36, v102 row_newbcast:12 row_mask:0xf bank_mask:0xc
	v_mov_b32_dpp v50, v36 row_newbcast:6 row_mask:0xf bank_mask:0x3
	v_mov_b32_dpp v50, v36 row_newbcast:14 row_mask:0xf bank_mask:0xc
	v_mov_b32_dpp v36, v36 row_newbcast:7 row_mask:0xf bank_mask:0x3
	v_mov_b32_dpp v36, v36 row_newbcast:15 row_mask:0xf bank_mask:0xc
	v_add_u32_e32 v51, v102, v60
	ds_read_b128 v[60:63], v37 offset:52240
	ds_read_b128 v[64:67], v51 offset:52240
	s_add_i32 s22, s22, 8
	v_add_u32_e32 v37, v102, v50
	v_add_u32_e32 v36, v102, v36
	ds_read_b128 v[68:71], v37 offset:52240
	ds_read_b128 v[74:77], v36 offset:52240
	s_waitcnt lgkmcnt(7)
	v_pk_fma_f16 v36, v73, v38, v52
	v_pk_fma_f16 v37, v73, v39, v53
	v_pk_fma_f16 v38, v73, v40, v54
	v_pk_fma_f16 v39, v73, v41, v55
	s_waitcnt lgkmcnt(6)
	v_pk_fma_f16 v38, v73, v44, v38
	v_pk_fma_f16 v39, v73, v45, v39
	v_pk_fma_f16 v37, v73, v43, v37
	v_pk_fma_f16 v36, v73, v42, v36
	s_waitcnt lgkmcnt(5)
	v_pk_fma_f16 v37, v73, v47, v37
	v_pk_fma_f16 v36, v73, v46, v36
	v_pk_fma_f16 v38, v73, v48, v38
	v_pk_fma_f16 v39, v73, v49, v39
	s_waitcnt lgkmcnt(4)
	v_pk_fma_f16 v38, v73, v58, v38
	v_pk_fma_f16 v39, v73, v59, v39
	v_pk_fma_f16 v37, v73, v57, v37
	v_pk_fma_f16 v36, v73, v56, v36
	s_waitcnt lgkmcnt(3)
	v_pk_fma_f16 v37, v73, v61, v37
	v_pk_fma_f16 v36, v73, v60, v36
	v_pk_fma_f16 v38, v73, v62, v38
	v_pk_fma_f16 v39, v73, v63, v39
	s_waitcnt lgkmcnt(2)
	v_pk_fma_f16 v38, v73, v66, v38
	v_pk_fma_f16 v39, v73, v67, v39
	v_pk_fma_f16 v37, v73, v65, v37
	v_pk_fma_f16 v36, v73, v64, v36
	s_waitcnt lgkmcnt(1)
	v_pk_fma_f16 v37, v73, v69, v37
	v_pk_fma_f16 v36, v73, v68, v36
	v_pk_fma_f16 v38, v73, v70, v38
	v_pk_fma_f16 v39, v73, v71, v39
	s_waitcnt lgkmcnt(0)
	v_pk_fma_f16 v54, v73, v76, v38
	v_pk_fma_f16 v55, v73, v77, v39
	v_pk_fma_f16 v53, v73, v75, v37
	v_pk_fma_f16 v52, v73, v74, v36

.LBB4_61:
	ds_write_b128 v104, v[52:55] offset:33792
	ds_read_b128 v[36:39], v105
	ds_read_b128 v[40:43], v103 offset:33792
	ds_read_b128 v[44:47], v105 offset:8448
	ds_read_b128 v[48:51], v105 offset:16896
	ds_read_b128 v[52:55], v105 offset:25344
	s_waitcnt lgkmcnt(3)
	v_mfma_f32_16x16x32_f16 v[36:39], v[36:39], v[40:43], 0
	s_waitcnt lgkmcnt(2)
	v_mfma_f32_16x16x32_f16 v[44:47], v[44:47], v[40:43], 0
	s_waitcnt lgkmcnt(1)
	v_mfma_f32_16x16x32_f16 v[48:51], v[48:51], v[40:43], 0
	s_waitcnt lgkmcnt(0)
	v_mfma_f32_16x16x32_f16 v[52:55], v[52:55], v[40:43], 0
	ds_read_b128 v[40:43], v105 offset:64
	ds_read_b128 v[56:59], v103 offset:33856
	ds_read_b128 v[60:63], v105 offset:8512
	ds_read_b128 v[64:67], v105 offset:16960
	s_waitcnt lgkmcnt(2)
	v_mfma_f32_16x16x32_f16 v[36:39], v[40:43], v[56:59], v[36:39]
	v_cmp_lt_i32_e32 vcc, 8, v108
	s_cmp_lg_u64 vcc, 0
	v_add_u32_dpp v32, v85, v102 row_newbcast:0 row_mask:0xf bank_mask:0x3
	v_add_u32_dpp v32, v85, v102 row_newbcast:8 row_mask:0xf bank_mask:0xc
	s_waitcnt lgkmcnt(1)
	v_mfma_f32_16x16x32_f16 v[40:43], v[60:63], v[56:59], v[44:47]
	ds_read_b128 v[60:63], v105 offset:25408
	ds_read_b128 v[68:71], v32 offset:52240
	s_waitcnt lgkmcnt(2)
	v_mfma_f32_16x16x32_f16 v[44:47], v[64:67], v[56:59], v[48:51]
	v_add_u32_dpp v64, v85, v102 row_newbcast:1 row_mask:0xf bank_mask:0x3
	v_add_u32_dpp v64, v85, v102 row_newbcast:9 row_mask:0xf bank_mask:0xc
	s_cselect_b64 s[22:23], -1, 0
	v_cmp_lt_i32_e64 s[6:7], 12, v108
	s_waitcnt lgkmcnt(1)
	v_mfma_f32_16x16x32_f16 v[48:51], v[60:63], v[56:59], v[52:55]
	v_add_u32_dpp v32, v85, v102 row_newbcast:2 row_mask:0xf bank_mask:0x3
	v_add_u32_dpp v32, v85, v102 row_newbcast:10 row_mask:0xf bank_mask:0xc
	s_nop 0
	ds_read_b128 v[76:79], v64 offset:52240
	ds_read_b128 v[72:75], v32 offset:52240
	v_add_u32_dpp v32, v85, v102 row_newbcast:3 row_mask:0xf bank_mask:0x3
	v_add_u32_dpp v32, v85, v102 row_newbcast:11 row_mask:0xf bank_mask:0xc
	v_add_u32_dpp v52, v85, v102 row_newbcast:4 row_mask:0xf bank_mask:0x3
	v_add_u32_dpp v52, v85, v102 row_newbcast:12 row_mask:0xf bank_mask:0xc
	ds_read_b128 v[80:83], v32 offset:52240
	ds_read_b128 v[52:55], v52 offset:52240
	v_add_u32_dpp v56, v85, v102 row_newbcast:5 row_mask:0xf bank_mask:0x3
	v_add_u32_dpp v56, v85, v102 row_newbcast:13 row_mask:0xf bank_mask:0xc
	v_add_u32_dpp v57, v85, v102 row_newbcast:6 row_mask:0xf bank_mask:0x3
	v_add_u32_dpp v57, v85, v102 row_newbcast:14 row_mask:0xf bank_mask:0xc
	ds_read_b128 v[60:63], v56 offset:52240
	ds_read_b128 v[64:67], v57 offset:52240
	v_add_u32_dpp v32, v85, v102 row_newbcast:7 row_mask:0xf bank_mask:0x3
	v_add_u32_dpp v32, v85, v102 row_newbcast:15 row_mask:0xf bank_mask:0xc
	ds_read_b128 v[56:59], v32 offset:52240
	s_cbranch_vccz .LBB4_63
	v_add_u32_dpp v0, v84, v102 row_newbcast:0 row_mask:0xf bank_mask:0x3
	v_add_u32_dpp v0, v84, v102 row_newbcast:8 row_mask:0xf bank_mask:0xc
	v_add_u32_dpp v8, v84, v102 row_newbcast:1 row_mask:0xf bank_mask:0x3
	v_add_u32_dpp v8, v84, v102 row_newbcast:9 row_mask:0xf bank_mask:0xc
	v_add_u32_dpp v16, v84, v102 row_newbcast:2 row_mask:0xf bank_mask:0x3
	v_add_u32_dpp v16, v84, v102 row_newbcast:10 row_mask:0xf bank_mask:0xc
	v_add_u32_dpp v24, v84, v102 row_newbcast:3 row_mask:0xf bank_mask:0x3
	v_add_u32_dpp v24, v84, v102 row_newbcast:11 row_mask:0xf bank_mask:0xc
	ds_read_b128 v[0:3], v0 offset:52240
	ds_read_b128 v[8:11], v8 offset:52240
	ds_read_b128 v[16:19], v16 offset:52240
	ds_read_b128 v[24:27], v24 offset:52240
.LBB4_63:
	s_cmp_lg_u64 s[6:7], 0
	s_cselect_b64 s[26:27], -1, 0
	s_cmp_eq_u64 s[6:7], 0
	s_cbranch_scc1 .LBB4_65
	v_add_u32_dpp v4, v84, v102 row_newbcast:4 row_mask:0xf bank_mask:0x3
	v_add_u32_dpp v4, v84, v102 row_newbcast:12 row_mask:0xf bank_mask:0xc
	v_add_u32_dpp v12, v84, v102 row_newbcast:5 row_mask:0xf bank_mask:0x3
	v_add_u32_dpp v12, v84, v102 row_newbcast:13 row_mask:0xf bank_mask:0xc
	v_add_u32_dpp v20, v84, v102 row_newbcast:6 row_mask:0xf bank_mask:0x3
	v_add_u32_dpp v20, v84, v102 row_newbcast:14 row_mask:0xf bank_mask:0xc
	v_add_u32_dpp v28, v84, v102 row_newbcast:7 row_mask:0xf bank_mask:0x3
	v_add_u32_dpp v28, v84, v102 row_newbcast:15 row_mask:0xf bank_mask:0xc
	ds_read_b128 v[4:7], v4 offset:52240
	ds_read_b128 v[12:15], v12 offset:52240
	ds_read_b128 v[20:23], v20 offset:52240
	ds_read_b128 v[28:31], v28 offset:52240

.LBB4_69:
	v_cmp_lt_i32_e32 vcc, 16, v108
	s_cbranch_vccz .LBB4_80
	v_cmp_lt_i32_e32 vcc, 20, v108
	v_add_u32_dpp v72, v109, v102 row_newbcast:0 row_mask:0xf bank_mask:0x3
	v_add_u32_dpp v72, v109, v102 row_newbcast:8 row_mask:0xf bank_mask:0xc
	v_add_u32_dpp v73, v109, v102 row_newbcast:1 row_mask:0xf bank_mask:0x3
	v_add_u32_dpp v73, v109, v102 row_newbcast:9 row_mask:0xf bank_mask:0xc
	ds_read_b128 v[84:87], v72 offset:52240
	ds_read_b128 v[80:83], v73 offset:52240
	v_add_u32_dpp v72, v109, v102 row_newbcast:2 row_mask:0xf bank_mask:0x3
	v_add_u32_dpp v72, v109, v102 row_newbcast:10 row_mask:0xf bank_mask:0xc
	v_add_u32_dpp v73, v109, v102 row_newbcast:3 row_mask:0xf bank_mask:0x3
	v_add_u32_dpp v73, v109, v102 row_newbcast:11 row_mask:0xf bank_mask:0xc
	ds_read_b128 v[76:79], v72 offset:52240
	ds_read_b128 v[72:75], v73 offset:52240
	s_cmp_lg_u64 vcc, 0
	s_cselect_b64 s[6:7], -1, 0
	s_cbranch_vccz .LBB4_72
	v_add_u32_dpp v52, v109, v102 row_newbcast:4 row_mask:0xf bank_mask:0x3
	v_add_u32_dpp v52, v109, v102 row_newbcast:12 row_mask:0xf bank_mask:0xc
	v_add_u32_dpp v58, v109, v102 row_newbcast:5 row_mask:0xf bank_mask:0x3
	v_add_u32_dpp v58, v109, v102 row_newbcast:13 row_mask:0xf bank_mask:0xc
	v_add_u32_dpp v56, v109, v102 row_newbcast:6 row_mask:0xf bank_mask:0x3
	v_add_u32_dpp v56, v109, v102 row_newbcast:14 row_mask:0xf bank_mask:0xc
	v_add_u32_dpp v57, v109, v102 row_newbcast:7 row_mask:0xf bank_mask:0x3
	v_add_u32_dpp v57, v109, v102 row_newbcast:15 row_mask:0xf bank_mask:0xc
	ds_read_b128 v[52:55], v52 offset:52240
	ds_read_b128 v[60:63], v58 offset:52240
	ds_read_b128 v[64:67], v56 offset:52240
	ds_read_b128 v[56:59], v57 offset:52240

.LBB4_75:
	s_waitcnt lgkmcnt(0)
	s_or_b64 exec, exec, s[6:7]
	s_nop 1
	v_add_u32_dpp v53, v52, v102 row_newbcast:0 row_mask:0xf bank_mask:0x3
	v_add_u32_dpp v53, v52, v102 row_newbcast:8 row_mask:0xf bank_mask:0xc
	v_add_u32_dpp v58, v52, v102 row_newbcast:1 row_mask:0xf bank_mask:0x3
	v_add_u32_dpp v58, v52, v102 row_newbcast:9 row_mask:0xf bank_mask:0xc
	ds_read_b128 v[54:57], v53 offset:52240
	ds_read_b128 v[58:61], v58 offset:52240
	v_add_u32_dpp v53, v52, v102 row_newbcast:2 row_mask:0xf bank_mask:0x3
	v_add_u32_dpp v53, v52, v102 row_newbcast:10 row_mask:0xf bank_mask:0xc
	v_add_u32_dpp v67, v52, v102 row_newbcast:3 row_mask:0xf bank_mask:0x3
	v_add_u32_dpp v67, v52, v102 row_newbcast:11 row_mask:0xf bank_mask:0xc
	v_mov_b32_dpp v76, v52 row_newbcast:5 row_mask:0xf bank_mask:0x3
	v_mov_b32_dpp v76, v52 row_newbcast:13 row_mask:0xf bank_mask:0xc
	ds_read_b128 v[62:65], v53 offset:52240
	ds_read_b128 v[72:75], v67 offset:52240
	v_add_u32_dpp v53, v52, v102 row_newbcast:4 row_mask:0xf bank_mask:0x3
	v_add_u32_dpp v53, v52, v102 row_newbcast:12 row_mask:0xf bank_mask:0xc
	v_mov_b32_dpp v66, v52 row_newbcast:6 row_mask:0xf bank_mask:0x3
	v_mov_b32_dpp v66, v52 row_newbcast:14 row_mask:0xf bank_mask:0xc
	v_mov_b32_dpp v52, v52 row_newbcast:7 row_mask:0xf bank_mask:0x3
	v_mov_b32_dpp v52, v52 row_newbcast:15 row_mask:0xf bank_mask:0xc
	v_add_u32_e32 v67, v102, v76
	ds_read_b128 v[76:79], v53 offset:52240
	ds_read_b128 v[80:83], v67 offset:52240
	s_add_i32 s22, s22, 8
	v_add_u32_e32 v53, v102, v66
	v_add_u32_e32 v52, v102, v52
	ds_read_b128 v[84:87], v53 offset:52240
	ds_read_b128 v[110:113], v52 offset:52240
	s_waitcnt lgkmcnt(7)
	v_pk_fma_f16 v52, v32, v54, v68
	v_pk_fma_f16 v53, v32, v55, v69
	v_pk_fma_f16 v54, v32, v56, v70
	v_pk_fma_f16 v55, v32, v57, v71
	s_waitcnt lgkmcnt(6)
	v_pk_fma_f16 v54, v32, v60, v54
	v_pk_fma_f16 v55, v32, v61, v55
	v_pk_fma_f16 v53, v32, v59, v53
	v_pk_fma_f16 v52, v32, v58, v52
	s_waitcnt lgkmcnt(5)
	v_pk_fma_f16 v53, v32, v63, v53
	v_pk_fma_f16 v52, v32, v62, v52
	v_pk_fma_f16 v54, v32, v64, v54
	v_pk_fma_f16 v55, v32, v65, v55
	s_waitcnt lgkmcnt(4)
	v_pk_fma_f16 v54, v32, v74, v54
	v_pk_fma_f16 v55, v32, v75, v55
	v_pk_fma_f16 v53, v32, v73, v53
	v_pk_fma_f16 v52, v32, v72, v52
	s_waitcnt lgkmcnt(3)
	v_pk_fma_f16 v53, v32, v77, v53
	v_pk_fma_f16 v52, v32, v76, v52
	v_pk_fma_f16 v54, v32, v78, v54
	v_pk_fma_f16 v55, v32, v79, v55
	s_waitcnt lgkmcnt(2)
	v_pk_fma_f16 v54, v32, v82, v54
	v_pk_fma_f16 v55, v32, v83, v55
	v_pk_fma_f16 v53, v32, v81, v53
	v_pk_fma_f16 v52, v32, v80, v52
	s_waitcnt lgkmcnt(1)
	v_pk_fma_f16 v53, v32, v85, v53
	v_pk_fma_f16 v52, v32, v84, v52
	v_pk_fma_f16 v54, v32, v86, v54
	v_pk_fma_f16 v55, v32, v87, v55
	s_waitcnt lgkmcnt(0)
	v_pk_fma_f16 v70, v32, v112, v54
	v_pk_fma_f16 v71, v32, v113, v55
	v_pk_fma_f16 v69, v32, v111, v53
	v_pk_fma_f16 v68, v32, v110, v52

.LBB4_80:
	ds_write_b128 v104, v[68:71] offset:33792
	ds_read_b128 v[52:55], v105 offset:128
	ds_read_b128 v[56:59], v103 offset:33792
	ds_read_b128 v[60:63], v105 offset:8576
	s_waitcnt lgkmcnt(1)
	v_mfma_f32_16x16x32_f16 v[36:39], v[52:55], v[56:59], v[36:39]
	ds_read_b128 v[52:55], v105 offset:17024
	s_waitcnt lgkmcnt(1)
	v_mfma_f32_16x16x32_f16 v[40:43], v[60:63], v[56:59], v[40:43]
	s_waitcnt lgkmcnt(0)
	v_mfma_f32_16x16x32_f16 v[44:47], v[52:55], v[56:59], v[44:47]
	ds_read_b128 v[52:55], v105 offset:25472
	s_waitcnt lgkmcnt(0)
	v_mfma_f32_16x16x32_f16 v[48:51], v[52:55], v[56:59], v[48:51]
	ds_read_b128 v[52:55], v105 offset:192
	ds_read_b128 v[56:59], v103 offset:33856
	ds_read_b128 v[60:63], v105 offset:8640
	v_cmp_lt_i32_e32 vcc, 8, v35
	s_waitcnt lgkmcnt(1)
	v_mfma_f32_16x16x32_f16 v[36:39], v[52:55], v[56:59], v[36:39]
	ds_read_b128 v[52:55], v105 offset:17088
	v_add_u32_dpp v32, v107, v102 row_newbcast:0 row_mask:0xf bank_mask:0x3
	v_add_u32_dpp v32, v107, v102 row_newbcast:8 row_mask:0xf bank_mask:0xc
	ds_read_b128 v[68:71], v32 offset:52240
	s_waitcnt lgkmcnt(2)
	v_mfma_f32_16x16x32_f16 v[40:43], v[60:63], v[56:59], v[40:43]
	ds_read_b128 v[60:63], v105 offset:25536
	v_add_u32_dpp v33, v107, v102 row_newbcast:1 row_mask:0xf bank_mask:0x3
	v_add_u32_dpp v33, v107, v102 row_newbcast:9 row_mask:0xf bank_mask:0xc
	s_cmp_lg_u64 vcc, 0
	s_waitcnt lgkmcnt(2)
	v_mfma_f32_16x16x32_f16 v[44:47], v[52:55], v[56:59], v[44:47]
	v_add_u32_dpp v32, v107, v102 row_newbcast:2 row_mask:0xf bank_mask:0x3
	v_add_u32_dpp v32, v107, v102 row_newbcast:10 row_mask:0xf bank_mask:0xc
	ds_read_b128 v[76:79], v33 offset:52240
	ds_read_b128 v[72:75], v32 offset:52240
	s_waitcnt lgkmcnt(2)
	v_mfma_f32_16x16x32_f16 v[48:51], v[60:63], v[56:59], v[48:51]
	v_add_u32_dpp v32, v107, v102 row_newbcast:3 row_mask:0xf bank_mask:0x3
	v_add_u32_dpp v32, v107, v102 row_newbcast:11 row_mask:0xf bank_mask:0xc
	v_add_u32_dpp v33, v107, v102 row_newbcast:4 row_mask:0xf bank_mask:0x3
	v_add_u32_dpp v33, v107, v102 row_newbcast:12 row_mask:0xf bank_mask:0xc
	ds_read_b128 v[80:83], v32 offset:52240
	ds_read_b128 v[52:55], v33 offset:52240
	s_cselect_b64 s[22:23], -1, 0
	v_add_u32_dpp v33, v107, v102 row_newbcast:5 row_mask:0xf bank_mask:0x3
	v_add_u32_dpp v33, v107, v102 row_newbcast:13 row_mask:0xf bank_mask:0xc
	v_add_u32_dpp v56, v107, v102 row_newbcast:6 row_mask:0xf bank_mask:0x3
	v_add_u32_dpp v56, v107, v102 row_newbcast:14 row_mask:0xf bank_mask:0xc
	ds_read_b128 v[60:63], v33 offset:52240
	ds_read_b128 v[64:67], v56 offset:52240
	v_add_u32_dpp v32, v107, v102 row_newbcast:7 row_mask:0xf bank_mask:0x3
	v_add_u32_dpp v32, v107, v102 row_newbcast:15 row_mask:0xf bank_mask:0xc
	ds_read_b128 v[56:59], v32 offset:52240
	v_cmp_lt_i32_e64 s[6:7], 12, v35
	s_cbranch_vccz .LBB4_82
	v_add_u32_dpp v0, v106, v102 row_newbcast:0 row_mask:0xf bank_mask:0x3
	v_add_u32_dpp v0, v106, v102 row_newbcast:8 row_mask:0xf bank_mask:0xc
	v_add_u32_dpp v8, v106, v102 row_newbcast:1 row_mask:0xf bank_mask:0x3
	v_add_u32_dpp v8, v106, v102 row_newbcast:9 row_mask:0xf bank_mask:0xc
	v_add_u32_dpp v16, v106, v102 row_newbcast:2 row_mask:0xf bank_mask:0x3
	v_add_u32_dpp v16, v106, v102 row_newbcast:10 row_mask:0xf bank_mask:0xc
	v_add_u32_dpp v24, v106, v102 row_newbcast:3 row_mask:0xf bank_mask:0x3
	v_add_u32_dpp v24, v106, v102 row_newbcast:11 row_mask:0xf bank_mask:0xc
	ds_read_b128 v[0:3], v0 offset:52240
	ds_read_b128 v[8:11], v8 offset:52240
	ds_read_b128 v[16:19], v16 offset:52240
	ds_read_b128 v[24:27], v24 offset:52240
.LBB4_82:
	s_cmp_lg_u64 s[6:7], 0
	s_cselect_b64 s[26:27], -1, 0
	s_cmp_eq_u64 s[6:7], 0
	s_cbranch_scc1 .LBB4_84
	v_add_u32_dpp v4, v106, v102 row_newbcast:4 row_mask:0xf bank_mask:0x3
	v_add_u32_dpp v4, v106, v102 row_newbcast:12 row_mask:0xf bank_mask:0xc
	v_add_u32_dpp v12, v106, v102 row_newbcast:5 row_mask:0xf bank_mask:0x3
	v_add_u32_dpp v12, v106, v102 row_newbcast:13 row_mask:0xf bank_mask:0xc
	v_add_u32_dpp v20, v106, v102 row_newbcast:6 row_mask:0xf bank_mask:0x3
	v_add_u32_dpp v20, v106, v102 row_newbcast:14 row_mask:0xf bank_mask:0xc
	v_add_u32_dpp v28, v106, v102 row_newbcast:7 row_mask:0xf bank_mask:0x3
	v_add_u32_dpp v28, v106, v102 row_newbcast:15 row_mask:0xf bank_mask:0xc
	ds_read_b128 v[4:7], v4 offset:52240
	ds_read_b128 v[12:15], v12 offset:52240
	ds_read_b128 v[20:23], v20 offset:52240
	ds_read_b128 v[28:31], v28 offset:52240

.LBB4_88:
	v_cmp_lt_i32_e32 vcc, 16, v35
	s_cbranch_vccz .LBB4_99
	v_cmp_lt_i32_e32 vcc, 20, v35
	v_add_u32_dpp v33, v95, v102 row_newbcast:0 row_mask:0xf bank_mask:0x3
	v_add_u32_dpp v33, v95, v102 row_newbcast:8 row_mask:0xf bank_mask:0xc
	v_add_u32_dpp v72, v95, v102 row_newbcast:1 row_mask:0xf bank_mask:0x3
	v_add_u32_dpp v72, v95, v102 row_newbcast:9 row_mask:0xf bank_mask:0xc
	ds_read_b128 v[84:87], v33 offset:52240
	ds_read_b128 v[80:83], v72 offset:52240
	v_add_u32_dpp v33, v95, v102 row_newbcast:2 row_mask:0xf bank_mask:0x3
	v_add_u32_dpp v33, v95, v102 row_newbcast:10 row_mask:0xf bank_mask:0xc
	v_add_u32_dpp v72, v95, v102 row_newbcast:3 row_mask:0xf bank_mask:0x3
	v_add_u32_dpp v72, v95, v102 row_newbcast:11 row_mask:0xf bank_mask:0xc
	ds_read_b128 v[76:79], v33 offset:52240
	ds_read_b128 v[72:75], v72 offset:52240
	s_cmp_lg_u64 vcc, 0
	s_cselect_b64 s[6:7], -1, 0
	s_cbranch_vccz .LBB4_91
	v_add_u32_dpp v33, v95, v102 row_newbcast:4 row_mask:0xf bank_mask:0x3
	v_add_u32_dpp v33, v95, v102 row_newbcast:12 row_mask:0xf bank_mask:0xc
	v_add_u32_dpp v58, v95, v102 row_newbcast:5 row_mask:0xf bank_mask:0x3
	v_add_u32_dpp v58, v95, v102 row_newbcast:13 row_mask:0xf bank_mask:0xc
	ds_read_b128 v[52:55], v33 offset:52240
	ds_read_b128 v[60:63], v58 offset:52240
	v_add_u32_dpp v33, v95, v102 row_newbcast:6 row_mask:0xf bank_mask:0x3
	v_add_u32_dpp v33, v95, v102 row_newbcast:14 row_mask:0xf bank_mask:0xc
	v_add_u32_dpp v56, v95, v102 row_newbcast:7 row_mask:0xf bank_mask:0x3
	v_add_u32_dpp v56, v95, v102 row_newbcast:15 row_mask:0xf bank_mask:0xc
	ds_read_b128 v[64:67], v33 offset:52240
	ds_read_b128 v[56:59], v56 offset:52240

.LBB5_13:
	s_waitcnt lgkmcnt(0)
	v_mov_b32_e32 v0, 0
	s_and_saveexec_b64 s[6:7], s[0:1]
	s_cbranch_execz .LBB5_17
	s_mov_b64 s[10:11], exec
	v_mbcnt_lo_u32_b32 v0, s10, 0
	v_mbcnt_hi_u32_b32 v0, s11, v0
	v_cmp_eq_u32_e32 vcc, 0, v0
	s_and_saveexec_b64 s[8:9], vcc
	s_bcnt1_i32_b64 s10, s[10:11]
	v_mov_b32_e32 v1, s10
	ds_add_rtn_u32 v1, v33, v1 offset:52224
	s_or_b64 exec, exec, s[8:9]
	s_waitcnt lgkmcnt(0)
	v_readfirstlane_b32 s8, v1
	s_nop 1
	v_add_u32_e32 v0, s8, v0
.LBB5_17:
	s_or_b64 exec, exec, s[6:7]
	v_readfirstlane_b32 s8, v0
	s_cmp_ge_i32 s8, s21
	s_mov_b64 s[6:7], -1
	s_cbranch_scc1 .LBB5_12
	s_lshl_b32 s33, s8, 3
	s_add_i32 s33, s33, s20
	v_add_u32_e32 v8, s33, v74
	v_cmp_gt_i32_e32 vcc, s28, v8
	v_mov_b32_e32 v0, 0
	v_mov_b32_e32 v6, 0
	v_mov_b32_e32 v7, 0
	v_mov_b32_e32 v4, 0
	v_mov_b32_e32 v5, 0
	s_and_saveexec_b64 s[6:7], vcc
	s_cbranch_execz .LBB5_20
	v_lshl_add_u32 v2, v8, 1, v8
	v_ashrrev_i32_e32 v3, 31, v2
	v_lshl_add_u64 v[2:3], v[2:3], 2, s[14:15]
	global_load_dwordx4 v[4:7], v[2:3], off

.Lp2_after_idx:
	s_waitcnt vmcnt(0)
	v_lshlrev_b32_e32 v9, 6, v9
	v_lshlrev_b32_e32 v8, 6, v8
	v_lshlrev_b32_e32 v60, 6, v60
	v_lshlrev_b32_e32 v59, 6, v59
	v_lshlrev_b32_e32 v62, 6, v62
	v_lshlrev_b32_e32 v89, 6, v89
	v_lshlrev_b32_e32 v88, 6, v88
	v_lshlrev_b32_e32 v86, 6, v86
	v_lshlrev_b32_e32 v7, 6, v7
	v_and_b32_e32 v9, 0x7fffc0, v9
	v_and_b32_e32 v8, 0x7fffc0, v8
	v_and_b32_e32 v60, 0x7fffc0, v60
	v_and_b32_e32 v59, 0x7fffc0, v59
	v_and_b32_e32 v62, 0x7fffc0, v62
	v_and_b32_e32 v89, 0x7fffc0, v89
	v_and_b32_e32 v88, 0x7fffc0, v88
	v_and_b32_e32 v86, 0x7fffc0, v86
	v_and_b32_e32 v7, 0x7fffc0, v7
	v_mov_b32_dpp v12, v9 row_newbcast:2 row_mask:0xf bank_mask:0x3
	v_mov_b32_dpp v12, v9 row_newbcast:10 row_mask:0xf bank_mask:0xc
	v_mov_b32_dpp v14, v9 row_newbcast:4 row_mask:0xf bank_mask:0x3
	v_mov_b32_dpp v14, v9 row_newbcast:12 row_mask:0xf bank_mask:0xc
	v_mov_b32_dpp v15, v9 row_newbcast:5 row_mask:0xf bank_mask:0x3
	v_mov_b32_dpp v15, v9 row_newbcast:13 row_mask:0xf bank_mask:0xc
	v_add_u32_dpp v10, v9, v81 row_newbcast:0 row_mask:0xf bank_mask:0x3
	v_add_u32_dpp v10, v9, v81 row_newbcast:8 row_mask:0xf bank_mask:0xc
	v_add_u32_dpp v11, v9, v81 row_newbcast:1 row_mask:0xf bank_mask:0x3
	v_add_u32_dpp v11, v9, v81 row_newbcast:9 row_mask:0xf bank_mask:0xc
	v_add_u32_dpp v13, v9, v81 row_newbcast:3 row_mask:0xf bank_mask:0x3
	v_add_u32_dpp v13, v9, v81 row_newbcast:11 row_mask:0xf bank_mask:0xc
	v_mov_b32_dpp v16, v9 row_newbcast:6 row_mask:0xf bank_mask:0x3
	v_mov_b32_dpp v16, v9 row_newbcast:14 row_mask:0xf bank_mask:0xc
	v_mov_b32_dpp v9, v9 row_newbcast:7 row_mask:0xf bank_mask:0x3
	v_mov_b32_dpp v9, v9 row_newbcast:15 row_mask:0xf bank_mask:0xc
	v_add_u32_e32 v12, v12, v81
	global_load_dwordx2 v[56:57], v10, s[30:31]
	global_load_dwordx2 v[52:53], v11, s[30:31]
	global_load_dwordx2 v[30:31], v12, s[30:31]
	global_load_dwordx2 v[24:25], v13, s[30:31]
	v_add_u32_e32 v10, v14, v81
	v_add_u32_e32 v11, v15, v81
	v_add_u32_e32 v9, v9, v81
	v_add_u32_e32 v12, v16, v81
	v_mov_b32_dpp v16, v8 row_newbcast:3 row_mask:0xf bank_mask:0x3
	v_mov_b32_dpp v16, v8 row_newbcast:11 row_mask:0xf bank_mask:0xc
	global_load_dwordx2 v[54:55], v10, s[30:31]
	global_load_dwordx2 v[50:51], v11, s[30:31]
	global_load_dwordx2 v[26:27], v12, s[30:31]
	global_load_dwordx2 v[20:21], v9, s[30:31]
	v_add_u32_dpp v9, v8, v81 row_newbcast:0 row_mask:0xf bank_mask:0x3
	v_add_u32_dpp v9, v8, v81 row_newbcast:8 row_mask:0xf bank_mask:0xc
	v_add_u32_dpp v10, v8, v81 row_newbcast:1 row_mask:0xf bank_mask:0x3
	v_add_u32_dpp v10, v8, v81 row_newbcast:9 row_mask:0xf bank_mask:0xc
	v_add_u32_dpp v11, v8, v81 row_newbcast:2 row_mask:0xf bank_mask:0x3
	v_add_u32_dpp v11, v8, v81 row_newbcast:10 row_mask:0xf bank_mask:0xc
	v_mov_b32_dpp v13, v8 row_newbcast:4 row_mask:0xf bank_mask:0x3
	v_mov_b32_dpp v13, v8 row_newbcast:12 row_mask:0xf bank_mask:0xc
	v_mov_b32_dpp v14, v8 row_newbcast:5 row_mask:0xf bank_mask:0x3
	v_mov_b32_dpp v14, v8 row_newbcast:13 row_mask:0xf bank_mask:0xc
	v_mov_b32_dpp v15, v8 row_newbcast:6 row_mask:0xf bank_mask:0x3
	v_mov_b32_dpp v15, v8 row_newbcast:14 row_mask:0xf bank_mask:0xc
	v_mov_b32_dpp v8, v8 row_newbcast:7 row_mask:0xf bank_mask:0x3
	v_mov_b32_dpp v8, v8 row_newbcast:15 row_mask:0xf bank_mask:0xc
	v_add_u32_e32 v12, v16, v81
	global_load_dwordx2 v[28:29], v9, s[30:31]
	global_load_dwordx2 v[22:23], v10, s[30:31]
	global_load_dwordx2 v[18:19], v11, s[30:31]
	global_load_dwordx2 v[16:17], v12, s[30:31]
	v_add_u32_e32 v9, v13, v81
	v_add_u32_e32 v10, v14, v81
	v_add_u32_e32 v11, v15, v81
	v_add_u32_e32 v8, v8, v81
	global_load_dwordx2 v[14:15], v9, s[30:31]
	global_load_dwordx2 v[12:13], v10, s[30:31]
	s_nop 0
	global_load_dwordx2 v[10:11], v11, s[30:31]
	s_nop 0
	global_load_dwordx2 v[8:9], v8, s[30:31]
	v_cmp_lt_i32_e32 vcc, 16, v58
	s_cmp_lg_u64 vcc, 0
	s_cselect_b64 s[36:37], -1, 0
	v_cmp_lt_i32_e64 s[10:11], 18, v58
	v_cmp_lt_i32_e64 s[8:9], 20, v58
	v_cmp_lt_i32_e64 s[6:7], 22, v58
	s_cbranch_vccz .LBB5_42
	v_add_u32_dpp v34, v60, v81 row_newbcast:0 row_mask:0xf bank_mask:0x3
	v_add_u32_dpp v34, v60, v81 row_newbcast:8 row_mask:0xf bank_mask:0xc
	v_add_u32_dpp v38, v60, v81 row_newbcast:1 row_mask:0xf bank_mask:0x3
	v_add_u32_dpp v38, v60, v81 row_newbcast:9 row_mask:0xf bank_mask:0xc
	global_load_dwordx2 v[34:35], v34, s[30:31]
	s_nop 0
	global_load_dwordx2 v[38:39], v38, s[30:31]
.LBB5_42:
	s_cmp_lg_u64 s[10:11], 0
	s_cselect_b64 s[34:35], -1, 0
	s_cmp_eq_u64 s[10:11], 0
	s_cbranch_scc1 .LBB5_44
	v_add_u32_dpp v36, v60, v81 row_newbcast:2 row_mask:0xf bank_mask:0x3
	v_add_u32_dpp v36, v60, v81 row_newbcast:10 row_mask:0xf bank_mask:0xc
	v_add_u32_dpp v42, v60, v81 row_newbcast:3 row_mask:0xf bank_mask:0x3
	v_add_u32_dpp v42, v60, v81 row_newbcast:11 row_mask:0xf bank_mask:0xc
	global_load_dwordx2 v[36:37], v36, s[30:31]
	s_nop 0
	global_load_dwordx2 v[42:43], v42, s[30:31]
.LBB5_44:
	s_cmp_lg_u64 s[8:9], 0
	s_cselect_b64 s[10:11], -1, 0
	s_cmp_eq_u64 s[8:9], 0
	s_cbranch_scc1 .LBB5_46
	v_add_u32_dpp v40, v60, v81 row_newbcast:4 row_mask:0xf bank_mask:0x3
	v_add_u32_dpp v40, v60, v81 row_newbcast:12 row_mask:0xf bank_mask:0xc
	v_add_u32_dpp v46, v60, v81 row_newbcast:5 row_mask:0xf bank_mask:0x3
	v_add_u32_dpp v46, v60, v81 row_newbcast:13 row_mask:0xf bank_mask:0xc
	global_load_dwordx2 v[40:41], v40, s[30:31]
	s_nop 0
	global_load_dwordx2 v[46:47], v46, s[30:31]
.LBB5_46:
	s_cmp_lg_u64 s[6:7], 0
	s_cselect_b64 s[8:9], -1, 0
	s_cmp_eq_u64 s[6:7], 0
	s_cbranch_scc1 .LBB5_48
	v_add_u32_dpp v44, v60, v81 row_newbcast:6 row_mask:0xf bank_mask:0x3
	v_add_u32_dpp v44, v60, v81 row_newbcast:14 row_mask:0xf bank_mask:0xc
	v_add_u32_dpp v48, v60, v81 row_newbcast:7 row_mask:0xf bank_mask:0x3
	v_add_u32_dpp v48, v60, v81 row_newbcast:15 row_mask:0xf bank_mask:0xc
	global_load_dwordx2 v[44:45], v44, s[30:31]
	s_nop 0
	global_load_dwordx2 v[48:49], v48, s[30:31]

.LBB5_57:
	s_waitcnt lgkmcnt(0)
	s_or_b64 exec, exec, s[6:7]
	s_nop 1
	v_add_u32_dpp v13, v12, v81 row_newbcast:0 row_mask:0xf bank_mask:0x3
	v_add_u32_dpp v13, v12, v81 row_newbcast:8 row_mask:0xf bank_mask:0xc
	v_add_u32_dpp v20, v12, v81 row_newbcast:3 row_mask:0xf bank_mask:0x3
	v_add_u32_dpp v20, v12, v81 row_newbcast:11 row_mask:0xf bank_mask:0xc
	global_load_dwordx2 v[14:15], v13, s[30:31]
	v_add_u32_dpp v24, v12, v81 row_newbcast:5 row_mask:0xf bank_mask:0x3
	v_add_u32_dpp v24, v12, v81 row_newbcast:13 row_mask:0xf bank_mask:0xc
	global_load_dwordx2 v[20:21], v20, s[30:31]
	v_add_u32_dpp v26, v12, v81 row_newbcast:7 row_mask:0xf bank_mask:0x3
	v_add_u32_dpp v26, v12, v81 row_newbcast:15 row_mask:0xf bank_mask:0xc
	global_load_dwordx2 v[24:25], v24, s[30:31]
	v_add_u32_dpp v16, v12, v81 row_newbcast:1 row_mask:0xf bank_mask:0x3
	v_add_u32_dpp v16, v12, v81 row_newbcast:9 row_mask:0xf bank_mask:0xc
	global_load_dwordx2 v[16:17], v16, s[30:31]
	v_add_u32_dpp v13, v12, v81 row_newbcast:2 row_mask:0xf bank_mask:0x3
	v_add_u32_dpp v13, v12, v81 row_newbcast:10 row_mask:0xf bank_mask:0xc
	global_load_dwordx2 v[18:19], v13, s[30:31]
	global_load_dwordx2 v[26:27], v26, s[30:31]
	s_add_i32 s8, s8, 8
	v_add_u32_dpp v13, v12, v81 row_newbcast:4 row_mask:0xf bank_mask:0x3
	v_add_u32_dpp v13, v12, v81 row_newbcast:12 row_mask:0xf bank_mask:0xc
	global_load_dwordx2 v[22:23], v13, s[30:31]
	v_mov_b32_dpp v13, v12 row_newbcast:6 row_mask:0xf bank_mask:0x3
	v_mov_b32_dpp v13, v12 row_newbcast:14 row_mask:0xf bank_mask:0xc
	v_add_u32_e32 v12, v13, v81
	global_load_dwordx2 v[12:13], v12, s[30:31]
	s_waitcnt vmcnt(7)
	v_cvt_scalef32_pk_f16_fp8 v28, v14, 1.0
	v_cvt_scalef32_pk_f16_fp8 v14, v14, 1.0 op_sel:[1,0,0]
	v_cvt_scalef32_pk_f16_fp8 v29, v15, 1.0
	v_cvt_scalef32_pk_f16_fp8 v15, v15, 1.0 op_sel:[1,0,0]
	v_pk_fma_f16 v28, v60, v28, v8
	v_pk_fma_f16 v14, v60, v14, v9
	v_pk_fma_f16 v29, v60, v29, v10
	s_waitcnt vmcnt(4)
	v_cvt_scalef32_pk_f16_fp8 v30, v16, 1.0
	v_cvt_scalef32_pk_f16_fp8 v16, v16, 1.0 op_sel:[1,0,0]
	v_cvt_scalef32_pk_f16_fp8 v31, v17, 1.0
	v_cvt_scalef32_pk_f16_fp8 v17, v17, 1.0 op_sel:[1,0,0]
	v_pk_fma_f16 v15, v60, v15, v11
	s_waitcnt vmcnt(3)
	v_cvt_scalef32_pk_f16_fp8 v50, v18, 1.0
	v_cvt_scalef32_pk_f16_fp8 v18, v18, 1.0 op_sel:[1,0,0]
	v_cvt_scalef32_pk_f16_fp8 v51, v19, 1.0
	v_cvt_scalef32_pk_f16_fp8 v19, v19, 1.0 op_sel:[1,0,0]
	v_pk_fma_f16 v15, v60, v17, v15
	v_pk_fma_f16 v17, v60, v31, v29
	v_pk_fma_f16 v14, v60, v16, v14
	v_pk_fma_f16 v16, v60, v30, v28
	v_cvt_scalef32_pk_f16_fp8 v52, v20, 1.0
	v_cvt_scalef32_pk_f16_fp8 v20, v20, 1.0 op_sel:[1,0,0]
	v_cvt_scalef32_pk_f16_fp8 v53, v21, 1.0
	v_cvt_scalef32_pk_f16_fp8 v21, v21, 1.0 op_sel:[1,0,0]
	v_pk_fma_f16 v16, v60, v50, v16
	v_pk_fma_f16 v14, v60, v18, v14
	v_pk_fma_f16 v17, v60, v51, v17
	v_pk_fma_f16 v15, v60, v19, v15
	s_waitcnt vmcnt(1)
	v_cvt_scalef32_pk_f16_fp8 v54, v22, 1.0
	v_cvt_scalef32_pk_f16_fp8 v22, v22, 1.0 op_sel:[1,0,0]
	v_cvt_scalef32_pk_f16_fp8 v55, v23, 1.0
	v_cvt_scalef32_pk_f16_fp8 v23, v23, 1.0 op_sel:[1,0,0]
	v_pk_fma_f16 v15, v60, v21, v15
	v_pk_fma_f16 v17, v60, v53, v17
	v_pk_fma_f16 v14, v60, v20, v14
	v_pk_fma_f16 v16, v60, v52, v16
	v_cvt_scalef32_pk_f16_fp8 v56, v24, 1.0
	v_cvt_scalef32_pk_f16_fp8 v24, v24, 1.0 op_sel:[1,0,0]
	v_cvt_scalef32_pk_f16_fp8 v57, v25, 1.0
	v_cvt_scalef32_pk_f16_fp8 v25, v25, 1.0 op_sel:[1,0,0]
	v_pk_fma_f16 v16, v60, v54, v16
	v_pk_fma_f16 v14, v60, v22, v14
	v_pk_fma_f16 v17, v60, v55, v17
	v_pk_fma_f16 v15, v60, v23, v15
	s_waitcnt vmcnt(0)
	v_cvt_scalef32_pk_f16_fp8 v61, v12, 1.0
	v_cvt_scalef32_pk_f16_fp8 v12, v12, 1.0 op_sel:[1,0,0]
	v_cvt_scalef32_pk_f16_fp8 v63, v13, 1.0
	v_cvt_scalef32_pk_f16_fp8 v13, v13, 1.0 op_sel:[1,0,0]
	v_pk_fma_f16 v15, v60, v25, v15
	v_pk_fma_f16 v17, v60, v57, v17
	v_pk_fma_f16 v14, v60, v24, v14
	v_pk_fma_f16 v16, v60, v56, v16
	v_cvt_scalef32_pk_f16_fp8 v64, v26, 1.0
	v_cvt_scalef32_pk_f16_fp8 v26, v26, 1.0 op_sel:[1,0,0]
	v_cvt_scalef32_pk_f16_fp8 v65, v27, 1.0
	v_cvt_scalef32_pk_f16_fp8 v27, v27, 1.0 op_sel:[1,0,0]
	v_pk_fma_f16 v16, v60, v61, v16
	v_pk_fma_f16 v12, v60, v12, v14
	v_pk_fma_f16 v14, v60, v63, v17
	v_pk_fma_f16 v13, v60, v13, v15
	v_pk_fma_f16 v14, v60, v65, v14
	v_pk_fma_f16 v15, v60, v27, v13
	v_pk_fma_f16 v13, v60, v26, v12
	v_pk_fma_f16 v12, v60, v64, v16
.LBB5_58:
	s_waitcnt lgkmcnt(0)
	s_nop 0
	v_mov_b64_e32 v[8:9], v[12:13]
	v_mov_b64_e32 v[10:11], v[14:15]
	v_cmp_lt_i32_e32 vcc, s8, v58
	s_cbranch_vccz .LBB5_61
	v_add_u32_e32 v12, s8, v75
	v_cmp_lt_i32_e32 vcc, v12, v58
	v_mov_b32_e32 v12, 0x61a800
	s_and_saveexec_b64 s[6:7], vcc
	s_cbranch_execz .LBB5_57
	v_add_u32_e32 v12, s8, v4
	v_ashrrev_i32_e32 v13, 31, v12
	v_lshl_add_u64 v[12:13], v[12:13], 2, s[26:27]
	global_load_dword v12, v[12:13], off
	s_waitcnt vmcnt(0)
	v_lshlrev_b32_e32 v12, 6, v12
	v_and_b32_e32 v12, 0x7fffc0, v12
	s_branch .LBB5_57
.LBB5_61:
	s_cbranch_execz .LBB5_58
	ds_write_b128 v82, v[8:11] offset:33792
	ds_read_b128 v[8:11], v83
	ds_read_b128 v[12:15], v80 offset:33792
	ds_read_b128 v[16:19], v83 offset:8448
	ds_read_b128 v[20:23], v83 offset:16896
	ds_read_b128 v[24:27], v83 offset:25344
	s_waitcnt lgkmcnt(3)
	v_mfma_f32_16x16x32_f16 v[8:11], v[8:11], v[12:15], 0
	s_waitcnt lgkmcnt(2)
	v_mfma_f32_16x16x32_f16 v[16:19], v[16:19], v[12:15], 0
	s_waitcnt lgkmcnt(1)
	v_mfma_f32_16x16x32_f16 v[20:23], v[20:23], v[12:15], 0
	s_waitcnt lgkmcnt(0)
	v_mfma_f32_16x16x32_f16 v[90:93], v[24:27], v[12:15], 0
	ds_read_b128 v[12:15], v83 offset:64
	ds_read_b128 v[94:97], v80 offset:33856
	ds_read_b128 v[24:27], v83 offset:8512
	ds_read_b128 v[98:101], v83 offset:16960
	s_waitcnt lgkmcnt(2)
	v_mfma_f32_16x16x32_f16 v[8:11], v[12:15], v[94:97], v[8:11]
	v_add_u32_dpp v4, v59, v81 row_newbcast:0 row_mask:0xf bank_mask:0x3
	v_add_u32_dpp v4, v59, v81 row_newbcast:8 row_mask:0xf bank_mask:0xc
	s_waitcnt lgkmcnt(1)
	v_mfma_f32_16x16x32_f16 v[12:15], v[24:27], v[94:97], v[16:19]
	v_mov_b32_dpp v24, v59 row_newbcast:5 row_mask:0xf bank_mask:0x3
	v_mov_b32_dpp v24, v59 row_newbcast:13 row_mask:0xf bank_mask:0xc
	v_mov_b32_dpp v25, v59 row_newbcast:6 row_mask:0xf bank_mask:0x3
	v_mov_b32_dpp v25, v59 row_newbcast:14 row_mask:0xf bank_mask:0xc
	v_mov_b32_dpp v26, v59 row_newbcast:7 row_mask:0xf bank_mask:0x3
	v_mov_b32_dpp v26, v59 row_newbcast:15 row_mask:0xf bank_mask:0xc
	v_mov_b32_dpp v19, v59 row_newbcast:4 row_mask:0xf bank_mask:0x3
	v_mov_b32_dpp v19, v59 row_newbcast:12 row_mask:0xf bank_mask:0xc
	v_add_u32_dpp v16, v59, v81 row_newbcast:1 row_mask:0xf bank_mask:0x3
	v_add_u32_dpp v16, v59, v81 row_newbcast:9 row_mask:0xf bank_mask:0xc
	v_add_u32_dpp v17, v59, v81 row_newbcast:2 row_mask:0xf bank_mask:0x3
	v_add_u32_dpp v17, v59, v81 row_newbcast:10 row_mask:0xf bank_mask:0xc
	v_add_u32_dpp v18, v59, v81 row_newbcast:3 row_mask:0xf bank_mask:0x3
	v_add_u32_dpp v18, v59, v81 row_newbcast:11 row_mask:0xf bank_mask:0xc
	global_load_dwordx2 v[72:73], v4, s[30:31]
	global_load_dwordx2 v[68:69], v16, s[30:31]
	global_load_dwordx2 v[64:65], v17, s[30:31]
	global_load_dwordx2 v[58:59], v18, s[30:31]
	v_add_u32_e32 v4, v19, v81
	v_add_u32_e32 v16, v24, v81
	v_add_u32_e32 v17, v25, v81
	v_add_u32_e32 v18, v26, v81
	global_load_dwordx2 v[70:71], v4, s[30:31]
	global_load_dwordx2 v[66:67], v16, s[30:31]
	global_load_dwordx2 v[60:61], v17, s[30:31]
	global_load_dwordx2 v[54:55], v18, s[30:31]
	v_add_u32_dpp v4, v62, v81 row_newbcast:0 row_mask:0xf bank_mask:0x3
	v_add_u32_dpp v4, v62, v81 row_newbcast:8 row_mask:0xf bank_mask:0xc
	v_mov_b32_dpp v19, v62 row_newbcast:4 row_mask:0xf bank_mask:0x3
	v_mov_b32_dpp v19, v62 row_newbcast:12 row_mask:0xf bank_mask:0xc
	v_add_u32_dpp v16, v62, v81 row_newbcast:1 row_mask:0xf bank_mask:0x3
	v_add_u32_dpp v16, v62, v81 row_newbcast:9 row_mask:0xf bank_mask:0xc
	v_add_u32_dpp v17, v62, v81 row_newbcast:2 row_mask:0xf bank_mask:0x3
	v_add_u32_dpp v17, v62, v81 row_newbcast:10 row_mask:0xf bank_mask:0xc
	v_add_u32_dpp v18, v62, v81 row_newbcast:3 row_mask:0xf bank_mask:0x3
	v_add_u32_dpp v18, v62, v81 row_newbcast:11 row_mask:0xf bank_mask:0xc
	v_mov_b32_dpp v24, v62 row_newbcast:5 row_mask:0xf bank_mask:0x3
	v_mov_b32_dpp v24, v62 row_newbcast:13 row_mask:0xf bank_mask:0xc
	v_mov_b32_dpp v25, v62 row_newbcast:6 row_mask:0xf bank_mask:0x3
	v_mov_b32_dpp v25, v62 row_newbcast:14 row_mask:0xf bank_mask:0xc
	v_mov_b32_dpp v26, v62 row_newbcast:7 row_mask:0xf bank_mask:0x3
	v_mov_b32_dpp v26, v62 row_newbcast:15 row_mask:0xf bank_mask:0xc
	global_load_dwordx2 v[62:63], v4, s[30:31]
	global_load_dwordx2 v[56:57], v16, s[30:31]
	global_load_dwordx2 v[52:53], v17, s[30:31]
	global_load_dwordx2 v[50:51], v18, s[30:31]
	v_add_u32_e32 v4, v19, v81
	v_add_u32_e32 v16, v24, v81
	v_add_u32_e32 v17, v25, v81
	v_add_u32_e32 v18, v26, v81
	global_load_dwordx2 v[30:31], v4, s[30:31]
	global_load_dwordx2 v[28:29], v16, s[30:31]
	global_load_dwordx2 v[26:27], v17, s[30:31]
	global_load_dwordx2 v[24:25], v18, s[30:31]
	s_waitcnt lgkmcnt(0)
	v_mfma_f32_16x16x32_f16 v[16:19], v[98:101], v[94:97], v[20:23]
	v_cmp_lt_i32_e32 vcc, 16, v87
	s_cmp_lg_u64 vcc, 0
	s_cselect_b64 s[36:37], -1, 0
	ds_read_b128 v[20:23], v83 offset:25408
	s_waitcnt lgkmcnt(0)
	v_mfma_f32_16x16x32_f16 v[20:23], v[20:23], v[94:97], v[90:93]
	v_cmp_lt_i32_e64 s[10:11], 18, v87
	v_cmp_lt_i32_e64 s[8:9], 20, v87
	v_cmp_lt_i32_e64 s[6:7], 22, v87
	s_cbranch_vccz .LBB5_64
	v_add_u32_dpp v4, v89, v81 row_newbcast:0 row_mask:0xf bank_mask:0x3
	v_add_u32_dpp v4, v89, v81 row_newbcast:8 row_mask:0xf bank_mask:0xc
	v_add_u32_dpp v38, v89, v81 row_newbcast:1 row_mask:0xf bank_mask:0x3
	v_add_u32_dpp v38, v89, v81 row_newbcast:9 row_mask:0xf bank_mask:0xc
	global_load_dwordx2 v[34:35], v4, s[30:31]
	s_nop 0
	global_load_dwordx2 v[38:39], v38, s[30:31]
.LBB5_64:
	s_cmp_lg_u64 s[10:11], 0
	s_cselect_b64 s[34:35], -1, 0
	s_cmp_eq_u64 s[10:11], 0
	s_cbranch_scc1 .LBB5_66
	v_add_u32_dpp v4, v89, v81 row_newbcast:2 row_mask:0xf bank_mask:0x3
	v_add_u32_dpp v4, v89, v81 row_newbcast:10 row_mask:0xf bank_mask:0xc
	v_add_u32_dpp v42, v89, v81 row_newbcast:3 row_mask:0xf bank_mask:0x3
	v_add_u32_dpp v42, v89, v81 row_newbcast:11 row_mask:0xf bank_mask:0xc
	global_load_dwordx2 v[36:37], v4, s[30:31]
	s_nop 0
	global_load_dwordx2 v[42:43], v42, s[30:31]
.LBB5_66:
	s_cmp_lg_u64 s[8:9], 0
	s_cselect_b64 s[10:11], -1, 0
	s_cmp_eq_u64 s[8:9], 0
	s_cbranch_scc1 .LBB5_68
	v_add_u32_dpp v4, v89, v81 row_newbcast:4 row_mask:0xf bank_mask:0x3
	v_add_u32_dpp v4, v89, v81 row_newbcast:12 row_mask:0xf bank_mask:0xc
	v_add_u32_dpp v46, v89, v81 row_newbcast:5 row_mask:0xf bank_mask:0x3
	v_add_u32_dpp v46, v89, v81 row_newbcast:13 row_mask:0xf bank_mask:0xc
	global_load_dwordx2 v[40:41], v4, s[30:31]
	s_nop 0
	global_load_dwordx2 v[46:47], v46, s[30:31]
.LBB5_68:
	s_cmp_lg_u64 s[6:7], 0
	s_cselect_b64 s[8:9], -1, 0
	s_cmp_eq_u64 s[6:7], 0
	s_cbranch_scc1 .LBB5_70
	v_add_u32_dpp v4, v89, v81 row_newbcast:6 row_mask:0xf bank_mask:0x3
	v_add_u32_dpp v4, v89, v81 row_newbcast:14 row_mask:0xf bank_mask:0xc
	v_add_u32_dpp v48, v89, v81 row_newbcast:7 row_mask:0xf bank_mask:0x3
	v_add_u32_dpp v48, v89, v81 row_newbcast:15 row_mask:0xf bank_mask:0xc
	global_load_dwordx2 v[44:45], v4, s[30:31]
	s_nop 0
	global_load_dwordx2 v[48:49], v48, s[30:31]

.LBB5_79:
	s_waitcnt lgkmcnt(0)
	s_or_b64 exec, exec, s[6:7]
	s_nop 1
	v_add_u32_dpp v29, v28, v81 row_newbcast:0 row_mask:0xf bank_mask:0x3
	v_add_u32_dpp v29, v28, v81 row_newbcast:8 row_mask:0xf bank_mask:0xc
	v_add_u32_dpp v54, v28, v81 row_newbcast:3 row_mask:0xf bank_mask:0x3
	v_add_u32_dpp v54, v28, v81 row_newbcast:11 row_mask:0xf bank_mask:0xc
	global_load_dwordx2 v[30:31], v29, s[30:31]
	v_add_u32_dpp v58, v28, v81 row_newbcast:5 row_mask:0xf bank_mask:0x3
	v_add_u32_dpp v58, v28, v81 row_newbcast:13 row_mask:0xf bank_mask:0xc
	global_load_dwordx2 v[54:55], v54, s[30:31]
	v_add_u32_dpp v60, v28, v81 row_newbcast:7 row_mask:0xf bank_mask:0x3
	v_add_u32_dpp v60, v28, v81 row_newbcast:15 row_mask:0xf bank_mask:0xc
	global_load_dwordx2 v[58:59], v58, s[30:31]
	v_add_u32_dpp v50, v28, v81 row_newbcast:1 row_mask:0xf bank_mask:0x3
	v_add_u32_dpp v50, v28, v81 row_newbcast:9 row_mask:0xf bank_mask:0xc
	global_load_dwordx2 v[50:51], v50, s[30:31]
	v_add_u32_dpp v29, v28, v81 row_newbcast:2 row_mask:0xf bank_mask:0x3
	v_add_u32_dpp v29, v28, v81 row_newbcast:10 row_mask:0xf bank_mask:0xc
	global_load_dwordx2 v[52:53], v29, s[30:31]
	global_load_dwordx2 v[60:61], v60, s[30:31]
	s_add_i32 s8, s8, 8
	v_add_u32_dpp v29, v28, v81 row_newbcast:4 row_mask:0xf bank_mask:0x3
	v_add_u32_dpp v29, v28, v81 row_newbcast:12 row_mask:0xf bank_mask:0xc
	global_load_dwordx2 v[56:57], v29, s[30:31]
	v_mov_b32_dpp v29, v28 row_newbcast:6 row_mask:0xf bank_mask:0x3
	v_mov_b32_dpp v29, v28 row_newbcast:14 row_mask:0xf bank_mask:0xc
	v_add_u32_e32 v28, v29, v81
	global_load_dwordx2 v[28:29], v28, s[30:31]
	s_waitcnt vmcnt(7)
	v_cvt_scalef32_pk_f16_fp8 v62, v30, 1.0
	v_cvt_scalef32_pk_f16_fp8 v30, v30, 1.0 op_sel:[1,0,0]
	v_cvt_scalef32_pk_f16_fp8 v63, v31, 1.0
	v_cvt_scalef32_pk_f16_fp8 v31, v31, 1.0 op_sel:[1,0,0]
	v_pk_fma_f16 v62, v4, v62, v24
	v_pk_fma_f16 v30, v4, v30, v25
	v_pk_fma_f16 v63, v4, v63, v26
	s_waitcnt vmcnt(4)
	v_cvt_scalef32_pk_f16_fp8 v64, v50, 1.0
	v_cvt_scalef32_pk_f16_fp8 v50, v50, 1.0 op_sel:[1,0,0]
	v_cvt_scalef32_pk_f16_fp8 v65, v51, 1.0
	v_cvt_scalef32_pk_f16_fp8 v51, v51, 1.0 op_sel:[1,0,0]
	v_pk_fma_f16 v31, v4, v31, v27
	s_waitcnt vmcnt(3)
	v_cvt_scalef32_pk_f16_fp8 v66, v52, 1.0
	v_cvt_scalef32_pk_f16_fp8 v52, v52, 1.0 op_sel:[1,0,0]
	v_cvt_scalef32_pk_f16_fp8 v67, v53, 1.0
	v_cvt_scalef32_pk_f16_fp8 v53, v53, 1.0 op_sel:[1,0,0]
	v_pk_fma_f16 v31, v4, v51, v31
	v_pk_fma_f16 v51, v4, v65, v63
	v_pk_fma_f16 v30, v4, v50, v30
	v_pk_fma_f16 v50, v4, v64, v62
	v_cvt_scalef32_pk_f16_fp8 v68, v54, 1.0
	v_cvt_scalef32_pk_f16_fp8 v54, v54, 1.0 op_sel:[1,0,0]
	v_cvt_scalef32_pk_f16_fp8 v69, v55, 1.0
	v_cvt_scalef32_pk_f16_fp8 v55, v55, 1.0 op_sel:[1,0,0]
	v_pk_fma_f16 v50, v4, v66, v50
	v_pk_fma_f16 v30, v4, v52, v30
	v_pk_fma_f16 v51, v4, v67, v51
	v_pk_fma_f16 v31, v4, v53, v31
	s_waitcnt vmcnt(1)
	v_cvt_scalef32_pk_f16_fp8 v70, v56, 1.0
	v_cvt_scalef32_pk_f16_fp8 v56, v56, 1.0 op_sel:[1,0,0]
	v_cvt_scalef32_pk_f16_fp8 v71, v57, 1.0
	v_cvt_scalef32_pk_f16_fp8 v57, v57, 1.0 op_sel:[1,0,0]
	v_pk_fma_f16 v31, v4, v55, v31
	v_pk_fma_f16 v51, v4, v69, v51
	v_pk_fma_f16 v30, v4, v54, v30
	v_pk_fma_f16 v50, v4, v68, v50
	v_cvt_scalef32_pk_f16_fp8 v72, v58, 1.0
	v_cvt_scalef32_pk_f16_fp8 v58, v58, 1.0 op_sel:[1,0,0]
	v_cvt_scalef32_pk_f16_fp8 v73, v59, 1.0
	v_cvt_scalef32_pk_f16_fp8 v59, v59, 1.0 op_sel:[1,0,0]
	v_pk_fma_f16 v50, v4, v70, v50
	v_pk_fma_f16 v30, v4, v56, v30
	v_pk_fma_f16 v51, v4, v71, v51
	v_pk_fma_f16 v31, v4, v57, v31
	s_waitcnt vmcnt(0)
	v_cvt_scalef32_pk_f16_fp8 v89, v28, 1.0
	v_cvt_scalef32_pk_f16_fp8 v28, v28, 1.0 op_sel:[1,0,0]
	v_cvt_scalef32_pk_f16_fp8 v90, v29, 1.0
	v_cvt_scalef32_pk_f16_fp8 v29, v29, 1.0 op_sel:[1,0,0]
	v_pk_fma_f16 v31, v4, v59, v31
	v_pk_fma_f16 v51, v4, v73, v51
	v_pk_fma_f16 v30, v4, v58, v30
	v_pk_fma_f16 v50, v4, v72, v50
	v_cvt_scalef32_pk_f16_fp8 v91, v60, 1.0
	v_cvt_scalef32_pk_f16_fp8 v60, v60, 1.0 op_sel:[1,0,0]
	v_cvt_scalef32_pk_f16_fp8 v92, v61, 1.0
	v_cvt_scalef32_pk_f16_fp8 v61, v61, 1.0 op_sel:[1,0,0]
	v_pk_fma_f16 v50, v4, v89, v50
	v_pk_fma_f16 v28, v4, v28, v30
	v_pk_fma_f16 v30, v4, v90, v51
	v_pk_fma_f16 v29, v4, v29, v31
	v_pk_fma_f16 v30, v4, v92, v30
	v_pk_fma_f16 v31, v4, v61, v29
	v_pk_fma_f16 v29, v4, v60, v28
	v_pk_fma_f16 v28, v4, v91, v50
.LBB5_80:
	s_waitcnt lgkmcnt(0)
	s_nop 0
	v_mov_b64_e32 v[24:25], v[28:29]
	v_mov_b64_e32 v[26:27], v[30:31]
	v_cmp_lt_i32_e32 vcc, s8, v87
	s_cbranch_vccz .LBB5_83
	v_add_u32_e32 v28, s8, v75
	v_cmp_lt_i32_e32 vcc, v28, v87
	v_mov_b32_e32 v28, 0x61a800
	s_and_saveexec_b64 s[6:7], vcc
	s_cbranch_execz .LBB5_79
	v_add_u32_e32 v28, s8, v5
	v_ashrrev_i32_e32 v29, 31, v28
	v_lshl_add_u64 v[28:29], v[28:29], 2, s[26:27]
	global_load_dword v28, v[28:29], off
	s_waitcnt vmcnt(0)
	v_lshlrev_b32_e32 v28, 6, v28
	v_and_b32_e32 v28, 0x7fffc0, v28
	s_branch .LBB5_79
.LBB5_83:
	s_cbranch_execz .LBB5_80
	ds_write_b128 v82, v[24:27] offset:33792
	ds_read_b128 v[24:27], v83 offset:128
	ds_read_b128 v[28:31], v80 offset:33792
	ds_read_b128 v[50:53], v83 offset:8576
	s_waitcnt lgkmcnt(1)
	v_mfma_f32_16x16x32_f16 v[8:11], v[24:27], v[28:31], v[8:11]
	ds_read_b128 v[24:27], v83 offset:17024
	s_waitcnt lgkmcnt(1)
	v_mfma_f32_16x16x32_f16 v[12:15], v[50:53], v[28:31], v[12:15]
	s_waitcnt lgkmcnt(0)
	v_mfma_f32_16x16x32_f16 v[16:19], v[24:27], v[28:31], v[16:19]
	ds_read_b128 v[24:27], v83 offset:25472
	s_waitcnt lgkmcnt(0)
	v_mfma_f32_16x16x32_f16 v[20:23], v[24:27], v[28:31], v[20:23]
	ds_read_b128 v[24:27], v83 offset:192
	ds_read_b128 v[90:93], v80 offset:33856
	ds_read_b128 v[28:31], v83 offset:8640
	ds_read_b128 v[94:97], v83 offset:17088
	s_waitcnt lgkmcnt(2)
	v_mfma_f32_16x16x32_f16 v[8:11], v[24:27], v[90:93], v[8:11]
	s_waitcnt lgkmcnt(1)
	v_mfma_f32_16x16x32_f16 v[12:15], v[28:31], v[90:93], v[12:15]
	v_add_u32_dpp v4, v88, v81 row_newbcast:0 row_mask:0xf bank_mask:0x3
	v_add_u32_dpp v4, v88, v81 row_newbcast:8 row_mask:0xf bank_mask:0xc
	v_add_u32_dpp v5, v88, v81 row_newbcast:1 row_mask:0xf bank_mask:0x3
	v_add_u32_dpp v5, v88, v81 row_newbcast:9 row_mask:0xf bank_mask:0xc
	v_add_u32_dpp v24, v88, v81 row_newbcast:2 row_mask:0xf bank_mask:0x3
	v_add_u32_dpp v24, v88, v81 row_newbcast:10 row_mask:0xf bank_mask:0xc
	v_add_u32_dpp v25, v88, v81 row_newbcast:3 row_mask:0xf bank_mask:0x3
	v_add_u32_dpp v25, v88, v81 row_newbcast:11 row_mask:0xf bank_mask:0xc
	global_load_dwordx2 v[70:71], v4, s[30:31]
	global_load_dwordx2 v[66:67], v5, s[30:31]
	global_load_dwordx2 v[62:63], v24, s[30:31]
	global_load_dwordx2 v[56:57], v25, s[30:31]
	v_add_u32_dpp v4, v88, v81 row_newbcast:4 row_mask:0xf bank_mask:0x3
	v_add_u32_dpp v4, v88, v81 row_newbcast:12 row_mask:0xf bank_mask:0xc
	v_add_u32_dpp v5, v88, v81 row_newbcast:5 row_mask:0xf bank_mask:0x3
	v_add_u32_dpp v5, v88, v81 row_newbcast:13 row_mask:0xf bank_mask:0xc
	v_add_u32_dpp v24, v88, v81 row_newbcast:6 row_mask:0xf bank_mask:0x3
	v_add_u32_dpp v24, v88, v81 row_newbcast:14 row_mask:0xf bank_mask:0xc
	v_add_u32_dpp v25, v88, v81 row_newbcast:7 row_mask:0xf bank_mask:0x3
	v_add_u32_dpp v25, v88, v81 row_newbcast:15 row_mask:0xf bank_mask:0xc
	global_load_dwordx2 v[68:69], v4, s[30:31]
	global_load_dwordx2 v[64:65], v5, s[30:31]
	global_load_dwordx2 v[58:59], v24, s[30:31]
	global_load_dwordx2 v[52:53], v25, s[30:31]
	v_add_u32_dpp v4, v86, v81 row_newbcast:0 row_mask:0xf bank_mask:0x3
	v_add_u32_dpp v4, v86, v81 row_newbcast:8 row_mask:0xf bank_mask:0xc
	v_add_u32_dpp v5, v86, v81 row_newbcast:1 row_mask:0xf bank_mask:0x3
	v_add_u32_dpp v5, v86, v81 row_newbcast:9 row_mask:0xf bank_mask:0xc
	v_add_u32_dpp v24, v86, v81 row_newbcast:2 row_mask:0xf bank_mask:0x3
	v_add_u32_dpp v24, v86, v81 row_newbcast:10 row_mask:0xf bank_mask:0xc
	v_add_u32_dpp v25, v86, v81 row_newbcast:3 row_mask:0xf bank_mask:0x3
	v_add_u32_dpp v25, v86, v81 row_newbcast:11 row_mask:0xf bank_mask:0xc
	global_load_dwordx2 v[60:61], v4, s[30:31]
	global_load_dwordx2 v[54:55], v5, s[30:31]
	global_load_dwordx2 v[50:51], v24, s[30:31]
	global_load_dwordx2 v[30:31], v25, s[30:31]
	v_add_u32_dpp v4, v86, v81 row_newbcast:4 row_mask:0xf bank_mask:0x3
	v_add_u32_dpp v4, v86, v81 row_newbcast:12 row_mask:0xf bank_mask:0xc
	v_add_u32_dpp v5, v86, v81 row_newbcast:5 row_mask:0xf bank_mask:0x3
	v_add_u32_dpp v5, v86, v81 row_newbcast:13 row_mask:0xf bank_mask:0xc
	v_add_u32_dpp v24, v86, v81 row_newbcast:6 row_mask:0xf bank_mask:0x3
	v_add_u32_dpp v24, v86, v81 row_newbcast:14 row_mask:0xf bank_mask:0xc
	v_add_u32_dpp v72, v86, v81 row_newbcast:7 row_mask:0xf bank_mask:0x3
	v_add_u32_dpp v72, v86, v81 row_newbcast:15 row_mask:0xf bank_mask:0xc
	global_load_dwordx2 v[28:29], v4, s[30:31]
	global_load_dwordx2 v[26:27], v5, s[30:31]
	s_nop 0
	global_load_dwordx2 v[24:25], v24, s[30:31]
	s_nop 0
	global_load_dwordx2 v[4:5], v72, s[30:31]
	ds_read_b128 v[86:89], v83 offset:25536
	s_waitcnt lgkmcnt(1)
	v_mfma_f32_16x16x32_f16 v[16:19], v[94:97], v[90:93], v[16:19]
	v_cmp_lt_i32_e32 vcc, 16, v85
	s_cmp_lg_u64 vcc, 0
	s_cselect_b64 s[36:37], -1, 0
	s_waitcnt lgkmcnt(0)
	v_mfma_f32_16x16x32_f16 v[20:23], v[86:89], v[90:93], v[20:23]
	v_cmp_lt_i32_e64 s[10:11], 18, v85
	v_cmp_lt_i32_e64 s[8:9], 20, v85
	v_cmp_lt_i32_e64 s[6:7], 22, v85
	s_cbranch_vccz .LBB5_86
	v_add_u32_dpp v34, v7, v81 row_newbcast:0 row_mask:0xf bank_mask:0x3
	v_add_u32_dpp v34, v7, v81 row_newbcast:8 row_mask:0xf bank_mask:0xc
	v_add_u32_dpp v38, v7, v81 row_newbcast:1 row_mask:0xf bank_mask:0x3
	v_add_u32_dpp v38, v7, v81 row_newbcast:9 row_mask:0xf bank_mask:0xc
	global_load_dwordx2 v[34:35], v34, s[30:31]
	s_nop 0
	global_load_dwordx2 v[38:39], v38, s[30:31]
.LBB5_86:
	s_cmp_lg_u64 s[10:11], 0
	s_cselect_b64 s[34:35], -1, 0
	s_cmp_eq_u64 s[10:11], 0
	s_cbranch_scc1 .LBB5_88
	v_add_u32_dpp v36, v7, v81 row_newbcast:2 row_mask:0xf bank_mask:0x3
	v_add_u32_dpp v36, v7, v81 row_newbcast:10 row_mask:0xf bank_mask:0xc
	v_add_u32_dpp v42, v7, v81 row_newbcast:3 row_mask:0xf bank_mask:0x3
	v_add_u32_dpp v42, v7, v81 row_newbcast:11 row_mask:0xf bank_mask:0xc
	global_load_dwordx2 v[36:37], v36, s[30:31]
	s_nop 0
	global_load_dwordx2 v[42:43], v42, s[30:31]
.LBB5_88:
	s_cmp_lg_u64 s[8:9], 0
	s_cselect_b64 s[10:11], -1, 0
	s_cmp_eq_u64 s[8:9], 0
	s_cbranch_scc1 .LBB5_90
	v_add_u32_dpp v40, v7, v81 row_newbcast:4 row_mask:0xf bank_mask:0x3
	v_add_u32_dpp v40, v7, v81 row_newbcast:12 row_mask:0xf bank_mask:0xc
	v_add_u32_dpp v46, v7, v81 row_newbcast:5 row_mask:0xf bank_mask:0x3
	v_add_u32_dpp v46, v7, v81 row_newbcast:13 row_mask:0xf bank_mask:0xc
	global_load_dwordx2 v[40:41], v40, s[30:31]
	s_nop 0
	global_load_dwordx2 v[46:47], v46, s[30:31]
.LBB5_90:
	s_cmp_lg_u64 s[6:7], 0
	s_cselect_b64 s[8:9], -1, 0
	s_cmp_eq_u64 s[6:7], 0
	s_cbranch_scc1 .LBB5_92
	v_mov_b32_dpp v44, v7 row_newbcast:6 row_mask:0xf bank_mask:0x3
	v_mov_b32_dpp v44, v7 row_newbcast:14 row_mask:0xf bank_mask:0xc
	v_mov_b32_dpp v7, v7 row_newbcast:7 row_mask:0xf bank_mask:0x3
	v_mov_b32_dpp v7, v7 row_newbcast:15 row_mask:0xf bank_mask:0xc
	v_add_u32_e32 v44, v44, v81
	v_add_u32_e32 v7, v7, v81
	global_load_dwordx2 v[44:45], v44, s[30:31]
	s_nop 0
	global_load_dwordx2 v[48:49], v7, s[30:31]

.LBB5_101:
	s_waitcnt lgkmcnt(0)
	s_or_b64 exec, exec, s[6:7]
	s_add_i32 s8, s8, 8
	v_add_u32_dpp v25, v24, v81 row_newbcast:0 row_mask:0xf bank_mask:0x3
	v_add_u32_dpp v25, v24, v81 row_newbcast:8 row_mask:0xf bank_mask:0xc
	v_add_u32_dpp v29, v24, v81 row_newbcast:1 row_mask:0xf bank_mask:0x3
	v_add_u32_dpp v29, v24, v81 row_newbcast:9 row_mask:0xf bank_mask:0xc
	global_load_dwordx2 v[26:27], v25, s[30:31]
	global_load_dwordx2 v[30:31], v29, s[30:31]
	v_add_u32_dpp v25, v24, v81 row_newbcast:2 row_mask:0xf bank_mask:0x3
	v_add_u32_dpp v25, v24, v81 row_newbcast:10 row_mask:0xf bank_mask:0xc
	v_add_u32_dpp v29, v24, v81 row_newbcast:3 row_mask:0xf bank_mask:0x3
	v_add_u32_dpp v29, v24, v81 row_newbcast:11 row_mask:0xf bank_mask:0xc
	global_load_dwordx2 v[50:51], v25, s[30:31]
	global_load_dwordx2 v[52:53], v29, s[30:31]
	v_add_u32_dpp v25, v24, v81 row_newbcast:4 row_mask:0xf bank_mask:0x3
	v_add_u32_dpp v25, v24, v81 row_newbcast:12 row_mask:0xf bank_mask:0xc
	v_add_u32_dpp v29, v24, v81 row_newbcast:5 row_mask:0xf bank_mask:0x3
	v_add_u32_dpp v29, v24, v81 row_newbcast:13 row_mask:0xf bank_mask:0xc
	global_load_dwordx2 v[54:55], v25, s[30:31]
	global_load_dwordx2 v[56:57], v29, s[30:31]
	v_mov_b32_dpp v25, v24 row_newbcast:6 row_mask:0xf bank_mask:0x3
	v_mov_b32_dpp v25, v24 row_newbcast:14 row_mask:0xf bank_mask:0xc
	v_mov_b32_dpp v29, v24 row_newbcast:7 row_mask:0xf bank_mask:0x3
	v_mov_b32_dpp v29, v24 row_newbcast:15 row_mask:0xf bank_mask:0xc
	v_add_u32_e32 v24, v25, v81
	global_load_dwordx2 v[24:25], v24, s[30:31]
	v_add_u32_e32 v29, v29, v81
	global_load_dwordx2 v[58:59], v29, s[30:31]
	s_waitcnt vmcnt(7)
	v_cvt_scalef32_pk_f16_fp8 v29, v26, 1.0
	v_cvt_scalef32_pk_f16_fp8 v26, v26, 1.0 op_sel:[1,0,0]
	v_cvt_scalef32_pk_f16_fp8 v60, v27, 1.0
	v_cvt_scalef32_pk_f16_fp8 v27, v27, 1.0 op_sel:[1,0,0]
	s_waitcnt vmcnt(6)
	v_cvt_scalef32_pk_f16_fp8 v61, v30, 1.0
	v_cvt_scalef32_pk_f16_fp8 v30, v30, 1.0 op_sel:[1,0,0]
	v_cvt_scalef32_pk_f16_fp8 v62, v31, 1.0
	v_cvt_scalef32_pk_f16_fp8 v31, v31, 1.0 op_sel:[1,0,0]
	v_pk_fma_f16 v29, v72, v29, v4
	v_pk_fma_f16 v26, v72, v26, v5
	v_pk_fma_f16 v60, v72, v60, v6
	v_pk_fma_f16 v27, v72, v27, v7
	s_waitcnt vmcnt(5)
	v_cvt_scalef32_pk_f16_fp8 v63, v50, 1.0
	v_cvt_scalef32_pk_f16_fp8 v50, v50, 1.0 op_sel:[1,0,0]
	v_cvt_scalef32_pk_f16_fp8 v64, v51, 1.0
	v_cvt_scalef32_pk_f16_fp8 v51, v51, 1.0 op_sel:[1,0,0]
	v_pk_fma_f16 v27, v72, v31, v27
	v_pk_fma_f16 v31, v72, v62, v60
	v_pk_fma_f16 v26, v72, v30, v26
	v_pk_fma_f16 v29, v72, v61, v29
	s_waitcnt vmcnt(4)
	v_cvt_scalef32_pk_f16_fp8 v65, v52, 1.0
	v_cvt_scalef32_pk_f16_fp8 v52, v52, 1.0 op_sel:[1,0,0]
	v_cvt_scalef32_pk_f16_fp8 v66, v53, 1.0
	v_cvt_scalef32_pk_f16_fp8 v53, v53, 1.0 op_sel:[1,0,0]
	v_pk_fma_f16 v29, v72, v63, v29
	v_pk_fma_f16 v26, v72, v50, v26
	v_pk_fma_f16 v30, v72, v64, v31
	v_pk_fma_f16 v27, v72, v51, v27
	s_waitcnt vmcnt(3)
	v_cvt_scalef32_pk_f16_fp8 v67, v54, 1.0
	v_cvt_scalef32_pk_f16_fp8 v54, v54, 1.0 op_sel:[1,0,0]
	v_cvt_scalef32_pk_f16_fp8 v68, v55, 1.0
	v_cvt_scalef32_pk_f16_fp8 v55, v55, 1.0 op_sel:[1,0,0]
	v_pk_fma_f16 v27, v72, v53, v27
	v_pk_fma_f16 v30, v72, v66, v30
	v_pk_fma_f16 v26, v72, v52, v26
	v_pk_fma_f16 v29, v72, v65, v29
	s_waitcnt vmcnt(2)
	v_cvt_scalef32_pk_f16_fp8 v69, v56, 1.0
	v_cvt_scalef32_pk_f16_fp8 v56, v56, 1.0 op_sel:[1,0,0]
	v_cvt_scalef32_pk_f16_fp8 v70, v57, 1.0
	v_cvt_scalef32_pk_f16_fp8 v57, v57, 1.0 op_sel:[1,0,0]
	v_pk_fma_f16 v29, v72, v67, v29
	v_pk_fma_f16 v26, v72, v54, v26
	v_pk_fma_f16 v30, v72, v68, v30
	v_pk_fma_f16 v27, v72, v55, v27
	s_waitcnt vmcnt(1)
	v_cvt_scalef32_pk_f16_fp8 v71, v24, 1.0
	v_cvt_scalef32_pk_f16_fp8 v24, v24, 1.0 op_sel:[1,0,0]
	v_cvt_scalef32_pk_f16_fp8 v73, v25, 1.0
	v_cvt_scalef32_pk_f16_fp8 v25, v25, 1.0 op_sel:[1,0,0]
	v_pk_fma_f16 v27, v72, v57, v27
	v_pk_fma_f16 v30, v72, v70, v30
	v_pk_fma_f16 v26, v72, v56, v26
	v_pk_fma_f16 v29, v72, v69, v29
	s_waitcnt vmcnt(0)
	v_cvt_scalef32_pk_f16_fp8 v86, v58, 1.0
	v_cvt_scalef32_pk_f16_fp8 v58, v58, 1.0 op_sel:[1,0,0]
	v_cvt_scalef32_pk_f16_fp8 v87, v59, 1.0
	v_cvt_scalef32_pk_f16_fp8 v59, v59, 1.0 op_sel:[1,0,0]
	v_pk_fma_f16 v29, v72, v71, v29
	v_pk_fma_f16 v24, v72, v24, v26
	v_pk_fma_f16 v26, v72, v73, v30
	v_pk_fma_f16 v25, v72, v25, v27
	v_pk_fma_f16 v26, v72, v87, v26
	v_pk_fma_f16 v27, v72, v59, v25
	v_pk_fma_f16 v25, v72, v58, v24
	v_pk_fma_f16 v24, v72, v86, v29
.LBB5_102:
	s_waitcnt lgkmcnt(0)
	s_nop 0
	v_mov_b64_e32 v[4:5], v[24:25]
	v_mov_b64_e32 v[6:7], v[26:27]
	v_cmp_lt_i32_e32 vcc, s8, v85
	s_cbranch_vccz .LBB5_105
	v_add_u32_e32 v24, s8, v75
	v_cmp_lt_i32_e32 vcc, v24, v85
	v_mov_b32_e32 v24, 0x61a800
	s_and_saveexec_b64 s[6:7], vcc
	s_cbranch_execz .LBB5_101
	v_add_u32_e32 v24, s8, v28
	v_ashrrev_i32_e32 v25, 31, v24
	v_lshl_add_u64 v[24:25], v[24:25], 2, s[26:27]
	global_load_dword v24, v[24:25], off
	s_waitcnt vmcnt(0)
	v_lshlrev_b32_e32 v24, 6, v24
	v_and_b32_e32 v24, 0x7fffc0, v24
	s_branch .LBB5_101
.LBB5_105:
	s_cbranch_execz .LBB5_102
	ds_write_b128 v82, v[4:7] offset:33792
	ds_read_b128 v[4:7], v83 offset:256
	ds_read_b128 v[24:27], v80 offset:33792
	ds_read_b128 v[28:31], v83 offset:8704
	s_waitcnt lgkmcnt(1)
	v_mfma_f32_16x16x32_f16 v[4:7], v[4:7], v[24:27], v[8:11]
	s_nop 2
	ds_read_b128 v[8:11], v83 offset:17152
	s_waitcnt lgkmcnt(1)
	v_mfma_f32_16x16x32_f16 v[12:15], v[28:31], v[24:27], v[12:15]
	s_waitcnt lgkmcnt(0)
	v_mfma_f32_16x16x32_f16 v[8:11], v[8:11], v[24:27], v[16:19]
	s_nop 2
	ds_read_b128 v[16:19], v83 offset:25600
	s_waitcnt lgkmcnt(0)
	v_mfma_f32_16x16x32_f16 v[16:19], v[16:19], v[24:27], v[20:23]
	s_nop 2
	ds_read_b128 v[20:23], v83 offset:320
	ds_read_b128 v[24:27], v80 offset:33856
	ds_read_b128 v[28:31], v83 offset:8768
	s_waitcnt lgkmcnt(1)
	v_mfma_f32_16x16x32_f16 v[4:7], v[20:23], v[24:27], v[4:7]
	ds_read_b128 v[20:23], v83 offset:17216
	s_waitcnt lgkmcnt(1)
	v_mfma_f32_16x16x32_f16 v[12:15], v[28:31], v[24:27], v[12:15]
	s_waitcnt lgkmcnt(0)
	v_mfma_f32_16x16x32_f16 v[8:11], v[20:23], v[24:27], v[8:11]
	ds_read_b128 v[20:23], v83 offset:25664
	ds_write_b128 v82, v[0:3] offset:33792
	s_waitcnt lgkmcnt(1)
	v_mfma_f32_16x16x32_f16 v[0:3], v[20:23], v[24:27], v[16:19]
	s_nop 2
	ds_read_b128 v[16:19], v83 offset:384
	ds_read_b128 v[20:23], v80 offset:33792
	ds_read_b128 v[24:27], v83 offset:8832
	s_waitcnt lgkmcnt(1)
	v_mfma_f32_16x16x32_f16 v[4:7], v[16:19], v[20:23], v[4:7]
	ds_read_b128 v[16:19], v83 offset:17280
	s_waitcnt lgkmcnt(1)
	v_mfma_f32_16x16x32_f16 v[12:15], v[24:27], v[20:23], v[12:15]
	s_waitcnt lgkmcnt(0)
	v_mfma_f32_16x16x32_f16 v[8:11], v[16:19], v[20:23], v[8:11]
	ds_read_b128 v[16:19], v83 offset:25728
	s_waitcnt lgkmcnt(0)
	v_mfma_f32_16x16x32_f16 v[0:3], v[16:19], v[20:23], v[0:3]
	ds_read_b128 v[16:19], v83 offset:448
	ds_read_b128 v[20:23], v80 offset:33856
	ds_read_b128 v[24:27], v83 offset:8896
	ds_read_b128 v[28:31], v83 offset:17344
	ds_read_b128 v[50:53], v83 offset:25792
	s_mov_b64 s[6:7], s[22:23]
	s_mov_b64 s[8:9], s[18:19]
	s_waitcnt lgkmcnt(1)
	v_mfma_f32_16x16x32_f16 v[8:11], v[28:31], v[20:23], v[8:11]
	s_nop 0
	s_waitcnt lgkmcnt(0)
	v_mfma_f32_16x16x32_f16 v[0:3], v[50:53], v[20:23], v[0:3]
	v_mfma_f32_16x16x32_f16 v[16:19], v[16:19], v[20:23], v[4:7]
	s_nop 2
	v_add_u32_e32 v6, s33, v77
	v_mfma_f32_16x16x32_f16 v[12:15], v[24:27], v[20:23], v[12:15]
	v_cmp_gt_i32_e32 vcc, s28, v6
	ds_read_b128 v[20:23], v32 offset:52240
	ds_read_b128 v[24:27], v32 offset:52496
	ds_read_b128 v[28:31], v32 offset:52752
	s_waitcnt lgkmcnt(2)
	v_add_f32_e32 v7, v16, v20
	s_waitcnt lgkmcnt(1)
	v_mov_b32_e32 v4, v24
	s_waitcnt lgkmcnt(0)
	v_mov_b32_e32 v5, v28
	v_add_f32_e32 v16, v17, v21
	v_add_f32_e32 v17, v18, v22
	v_add_f32_e32 v18, v19, v23
	v_max_f32_e32 v24, 0, v7
	v_max_f32_e32 v62, 0, v16
	v_max_f32_e32 v64, 0, v17
	v_max_f32_e32 v66, 0, v18
	ds_read_b128 v[16:19], v32 offset:52304
	ds_read_b128 v[20:23], v32 offset:52560
	ds_read_b128 v[50:53], v32 offset:52816
	s_waitcnt lgkmcnt(2)
	v_add_f32_e32 v7, v12, v16
	v_add_f32_e32 v12, v13, v17
	v_add_f32_e32 v13, v14, v18
	v_add_f32_e32 v14, v15, v19
	v_max_f32_e32 v68, 0, v7
	v_max_f32_e32 v70, 0, v12
	v_max_f32_e32 v72, 0, v13
	v_max_f32_e32 v86, 0, v14
	ds_read_b128 v[12:15], v32 offset:52368
	ds_read_b128 v[16:19], v32 offset:52624
	ds_read_b128 v[54:57], v32 offset:52880
	v_pk_fma_f32 v[88:89], v[4:5], v[24:25], 0 op_sel_hi:[1,0,0]
	v_mov_b32_e32 v28, v25
	v_mov_b32_e32 v24, v26
	v_mov_b32_e32 v25, v30
	v_mov_b32_e32 v30, v27
	s_waitcnt lgkmcnt(4)
	v_mov_b32_e32 v26, v20
	s_waitcnt lgkmcnt(3)
	v_mov_b32_e32 v27, v50
	v_mov_b32_e32 v50, v21
	v_mov_b32_e32 v20, v22
	v_mov_b32_e32 v21, v52
	v_mov_b32_e32 v52, v23
	v_pk_fma_f32 v[22:23], v[28:29], v[62:63], v[88:89] op_sel_hi:[1,0,1]
	v_mov_b32_e32 v4, v33
	v_pk_fma_f32 v[22:23], v[24:25], v[64:65], v[22:23] op_sel_hi:[1,0,1]
	v_mov_b32_e32 v5, v33
	v_pk_fma_f32 v[22:23], v[30:31], v[66:67], v[22:23] op_sel_hi:[1,0,1]
	s_waitcnt lgkmcnt(2)
	v_add_f32_e32 v7, v8, v12
	v_pk_fma_f32 v[22:23], v[26:27], v[68:69], v[22:23] op_sel_hi:[1,0,1]
	s_waitcnt lgkmcnt(1)
	v_mov_b32_e32 v8, v16
	v_pk_fma_f32 v[22:23], v[50:51], v[70:71], v[22:23] op_sel_hi:[1,0,1]
	v_add_f32_e32 v11, v11, v15
	v_pk_fma_f32 v[20:21], v[20:21], v[72:73], v[22:23] op_sel_hi:[1,0,1]
	v_add_f32_e32 v22, v9, v13
	v_pk_fma_f32 v[20:21], v[52:53], v[86:87], v[20:21] op_sel_hi:[1,0,1]
	v_add_f32_e32 v23, v10, v14
	s_waitcnt lgkmcnt(0)
	v_mov_b32_e32 v9, v54
	v_max_f32_e32 v10, 0, v7
	v_mov_b32_e32 v54, v17
	v_max_f32_e32 v14, 0, v22
	v_pk_fma_f32 v[8:9], v[8:9], v[10:11], v[20:21] op_sel_hi:[1,0,1]
	v_mov_b32_e32 v12, v18
	v_mov_b32_e32 v13, v56
	v_max_f32_e32 v16, 0, v23
	v_pk_fma_f32 v[8:9], v[54:55], v[14:15], v[8:9] op_sel_hi:[1,0,1]
	v_max_f32_e32 v22, 0, v11
	v_pk_fma_f32 v[8:9], v[12:13], v[16:17], v[8:9] op_sel_hi:[1,0,1]
	v_mov_b32_e32 v56, v19
	ds_read_b128 v[10:13], v32 offset:52432
	ds_read_b128 v[14:17], v32 offset:52688
	ds_read_b128 v[18:21], v32 offset:52944
	v_pk_fma_f32 v[22:23], v[56:57], v[22:23], v[8:9] op_sel_hi:[1,0,1]
	v_and_b32_e32 v24, 64, v84
	v_xor_b32_e32 v7, 16, v84
	v_add_u32_e32 v8, 64, v24
	v_cmp_lt_i32_e64 s[6:7], v7, v8
	s_and_b64 s[8:9], s[2:3], vcc
	s_waitcnt lgkmcnt(2)
	v_add_f32_e32 v9, v0, v10
	v_add_f32_e32 v11, v1, v11
	s_waitcnt lgkmcnt(1)
	v_mov_b32_e32 v0, v14
	s_waitcnt lgkmcnt(0)
	v_mov_b32_e32 v1, v18
	v_max_f32_e32 v10, 0, v9
	v_add_f32_e32 v24, v2, v12
	v_add_f32_e32 v13, v3, v13
	v_mov_b32_e32 v18, v15
	v_max_f32_e32 v12, 0, v11
	v_pk_fma_f32 v[0:1], v[0:1], v[10:11], v[22:23] op_sel_hi:[1,0,1]
	v_mov_b32_e32 v2, v16
	v_mov_b32_e32 v3, v20
	v_max_f32_e32 v14, 0, v24
	v_pk_fma_f32 v[0:1], v[18:19], v[12:13], v[0:1] op_sel_hi:[1,0,1]
	v_cndmask_b32_e64 v7, v84, v7, s[6:7]
	v_mov_b32_e32 v20, v17
	v_max_f32_e32 v16, 0, v13
	v_pk_fma_f32 v[0:1], v[2:3], v[14:15], v[0:1] op_sel_hi:[1,0,1]
	v_lshlrev_b32_e32 v7, 2, v7
	v_pk_fma_f32 v[0:1], v[20:21], v[16:17], v[0:1] op_sel_hi:[1,0,1]
	ds_bpermute_b32 v2, v7, v0
	ds_bpermute_b32 v3, v7, v1
	v_xor_b32_e32 v7, 32, v84
	v_cmp_lt_i32_e64 s[6:7], v7, v8
	v_mov_b32_e32 v10, -1
	s_waitcnt lgkmcnt(0)
	v_pk_add_f32 v[0:1], v[0:1], v[2:3]
	v_cndmask_b32_e64 v7, v84, v7, s[6:7]
	v_lshlrev_b32_e32 v7, 2, v7
	ds_bpermute_b32 v2, v7, v0
	ds_bpermute_b32 v3, v7, v1
	v_mov_b32_e32 v7, 0
	s_and_saveexec_b64 s[6:7], s[8:9]
	s_cbranch_execz .LBB5_108
	v_ashrrev_i32_e32 v7, 31, v6
	v_lshl_add_u64 v[4:5], v[6:7], 2, s[16:17]
	global_load_dword v10, v[4:5], off
	s_waitcnt lgkmcnt(0)
	v_pk_add_f32 v[4:5], v[0:1], v[2:3]
	v_mov_b32_e32 v7, 1.0

.LBB5_110:
	s_waitcnt lgkmcnt(0)
	s_or_b64 exec, exec, s[8:9]
	s_and_saveexec_b64 s[8:9], s[6:7]
	s_xor_b64 s[6:7], exec, s[8:9]
	s_cbranch_execz .LBB5_11
	s_branch .LBB5_117
